# GEMM phases: XCD-contiguous unit remap fed with the raw block index (was double-remapped via vcu): each XCD works on one contiguous id chunk, better L2 reuse of A/B tiles
# speedup vs baseline: 1.0266x; 1.0266x over previous
.LBB0_348:
	s_cmp_gt_i32 s6, 2
	s_cselect_b64 s[0:1], -1, 0
	s_cmp_lt_i32 s7, 3
	s_cselect_b64 s[2:3], -1, 0
	s_or_b64 s[0:1], s[0:1], s[2:3]
	s_and_b64 vcc, exec, s[0:1]
	s_cbranch_vccnz .LBB0_428
	s_mov_b32 s98, s88
	s_and_b32 s99, s88, 31
	s_lshl_b32 s99, s99, 3
	s_lshr_b32 s88, s88, 5
	s_or_b32 s88, s88, s99
	s_add_u32 s11, s94, 0x3d600000
	s_addc_u32 s30, s95, 0
	s_lshl_b32 s0, s88, 3
	v_readlane_b32 s1, v253, 20
	s_add_i32 s0, s0, s1
	s_cmpk_gt_i32 s0, 0xfff
	s_waitcnt vmcnt(3)
	v_mbcnt_lo_u32_b32 v0, -1, 0
	v_mbcnt_hi_u32_b32 v0, -1, v0
	s_cbranch_scc1 .LBB0_354
	v_readlane_b32 s3, v253, 20
	s_lshl_b32 s1, s88, 4
	s_lshl_b32 s3, s3, 1
	s_add_i32 s8, s1, s3
	s_ashr_i32 s1, s0, 31
	s_lshl_b32 s2, s90, 3
	s_lshl_b32 s9, s90, 4
	s_lshl_b64 s[4:5], s[0:1], 12
	v_lshlrev_b32_e32 v2, 6, v0
	s_add_u32 s4, s94, s4
	v_ashrrev_i32_e32 v3, 31, v2
	s_addc_u32 s5, s95, s5
	v_cmp_eq_u32_e32 vcc, 0, v0
	v_lshl_add_u64 v[0:1], s[4:5], 0, v[2:3]
	s_mov_b64 s[4:5], 0x37600000
	s_ashr_i32 s3, s2, 31
	v_lshl_add_u64 v[0:1], v[0:1], 0, s[4:5]
	s_lshl_b64 s[4:5], s[2:3], 12
	v_mov_b32_e32 v2, 0
	s_movk_i32 s1, 0x7fff
	v_mov_b32_e32 v3, 0x800000
	s_branch .LBB0_352

.LBB0_378:
	v_readlane_b32 s6, v253, 23
	v_readlane_b32 s7, v253, 24
	s_mov_b32 s88, s98
	s_cmp_gt_u32 s7, 3
	s_cbranch_scc0 .LBB0_428
	v_readlane_b32 s0, v253, 20
	s_waitcnt vmcnt(0)
	s_lshl_b32 s0, s0, 6
	s_sub_i32 s0, 0, s0
	s_waitcnt vmcnt(0)
	s_barrier
	v_mbcnt_lo_u32_b32 v0, -1, 0
	v_mbcnt_hi_u32_b32 v0, -1, v0
	s_nop 0
	v_cmp_eq_u32_e32 vcc, s0, v0
	s_and_saveexec_b64 s[0:1], vcc
	s_cbranch_execz .LBB0_427
	s_add_i32 s2, 0, 0x20160
	v_mov_b32_e32 v0, s2
	s_waitcnt vmcnt(0) expcnt(0) lgkmcnt(0)
	ds_read_b32 v2, v0
	s_add_i32 s2, 0, 0x20164
	v_mov_b32_e32 v0, s2
	ds_read_b32 v0, v0
	s_waitcnt lgkmcnt(1)
	v_cmp_ne_u32_e32 vcc, 0, v2
	s_cbranch_vccnz .LBB0_395
	v_readlane_b32 s2, v253, 0
	v_readlane_b32 s3, v253, 1
	s_load_dwordx2 s[6:7], s[2:3], 0x4
	s_add_u32 s2, s94, 0x4200
	s_addc_u32 s3, s95, 0
	s_add_u32 s4, s94, 0x4400
	s_addc_u32 s5, s95, 0
	s_waitcnt lgkmcnt(0)
	s_mul_i32 s33, s6, s90
	s_add_u32 s6, s94, 0x4500
	s_mul_i32 s33, s33, s7
	s_addc_u32 s7, s95, 0
	s_add_u32 s8, s94, 0x4600
	s_addc_u32 s9, s95, 0
	s_add_u32 s10, s94, 0x4700
	s_addc_u32 s11, s95, 0
	s_add_u32 s12, s94, 0x4800
	s_addc_u32 s13, s95, 0
	s_add_u32 s14, s94, 0x4900
	s_addc_u32 s15, s95, 0
	s_add_u32 s16, s94, 0x4a00
	s_addc_u32 s17, s95, 0
	s_add_u32 s18, s94, 0x4b00
	s_addc_u32 s19, s95, 0
	s_add_u32 s20, s94, 0x4c00
	s_addc_u32 s21, s95, 0
	s_add_u32 s22, s94, 0x4d00
	s_addc_u32 s23, s95, 0
	s_add_u32 s24, s94, 0x4e00
	s_addc_u32 s25, s95, 0
	s_add_u32 s26, s94, 0x4f00
	s_addc_u32 s27, s95, 0
	s_add_u32 s28, s94, 0x5000
	s_addc_u32 s29, s95, 0
	s_add_u32 s30, s94, 0x5100
	s_addc_u32 s31, s95, 0
	s_add_u32 s34, s94, 0x5200
	s_addc_u32 s35, s95, 0
	s_add_u32 s36, s94, 0x5300
	s_addc_u32 s37, s95, 0
	s_mov_b32 s44, 1
	v_mov_b32_e32 v16, 0
	s_branch .LBB0_383

.LBB0_428:
	s_cmp_gt_i32 s6, 3
	s_cselect_b64 s[0:1], -1, 0
	s_cmp_lt_i32 s7, 4
	s_cselect_b64 s[2:3], -1, 0
	s_or_b64 s[0:1], s[0:1], s[2:3]
	s_and_b64 vcc, exec, s[0:1]
	s_cbranch_vccnz .LBB0_545
	s_mov_b32 s98, s88
	s_and_b32 s99, s88, 31
	s_lshl_b32 s99, s99, 3
	s_lshr_b32 s88, s88, 5
	s_or_b32 s88, s88, s99
	s_cmpk_lt_i32 s88, 0x84
	s_cselect_b64 s[2:3], -1, 0
	s_cmpk_gt_i32 s88, 0x83
	s_waitcnt vmcnt(0)
	v_mbcnt_lo_u32_b32 v0, -1, 0
	v_mbcnt_hi_u32_b32 v0, -1, v0
	v_mbcnt_lo_u32_b32 v4, -1, 0
	v_mbcnt_hi_u32_b32 v4, -1, v4
	s_cbranch_scc1 .LBB0_432
	s_ashr_i32 s0, s88, 31
	s_lshr_b32 s0, s0, 29
	s_add_i32 s4, s88, s0
	s_and_b32 s0, s4, -8
	s_sub_i32 s5, s88, s0
	s_cmp_gt_i32 s5, 3
	s_cbranch_scc0 .LBB0_433
	s_lshl_b32 s0, s5, 4
	s_or_b32 s6, s0, 4
	s_cbranch_execz .LBB0_434
	s_branch .LBB0_435

.LBB0_495:
	v_readlane_b32 s6, v253, 23
	v_readlane_b32 s7, v253, 24
	s_mov_b32 s88, s98
	s_cmp_lt_u32 s7, 5
	s_cbranch_scc1 .LBB0_545
	v_readlane_b32 s0, v253, 20
	s_waitcnt vmcnt(0)
	s_lshl_b32 s0, s0, 6
	s_sub_i32 s0, 0, s0
	s_waitcnt vmcnt(0)
	s_barrier
	v_mbcnt_lo_u32_b32 v0, -1, 0
	v_mbcnt_hi_u32_b32 v0, -1, v0
	s_nop 0
	v_cmp_eq_u32_e32 vcc, s0, v0
	s_and_saveexec_b64 s[0:1], vcc
	s_cbranch_execz .LBB0_544
	s_add_i32 s2, 0, 0x20160
	v_mov_b32_e32 v0, s2
	s_waitcnt vmcnt(0) expcnt(0) lgkmcnt(0)
	ds_read_b32 v2, v0
	s_add_i32 s2, 0, 0x20164
	v_mov_b32_e32 v0, s2
	ds_read_b32 v0, v0
	s_waitcnt lgkmcnt(1)
	v_cmp_ne_u32_e32 vcc, 0, v2
	s_cbranch_vccnz .LBB0_512
	v_readlane_b32 s2, v253, 0
	v_readlane_b32 s3, v253, 1
	s_load_dwordx2 s[6:7], s[2:3], 0x4
	s_add_u32 s2, s94, 0x4200
	s_addc_u32 s3, s95, 0
	s_add_u32 s4, s94, 0x4400
	s_addc_u32 s5, s95, 0
	s_waitcnt lgkmcnt(0)
	s_mul_i32 s33, s6, s90
	s_add_u32 s6, s94, 0x4500
	s_mul_i32 s33, s33, s7
	s_addc_u32 s7, s95, 0
	s_add_u32 s8, s94, 0x4600
	s_addc_u32 s9, s95, 0
	s_add_u32 s10, s94, 0x4700
	s_addc_u32 s11, s95, 0
	s_add_u32 s12, s94, 0x4800
	s_addc_u32 s13, s95, 0
	s_add_u32 s14, s94, 0x4900
	s_addc_u32 s15, s95, 0
	s_add_u32 s16, s94, 0x4a00
	s_addc_u32 s17, s95, 0
	s_add_u32 s18, s94, 0x4b00
	s_addc_u32 s19, s95, 0
	s_add_u32 s20, s94, 0x4c00
	s_addc_u32 s21, s95, 0
	s_add_u32 s22, s94, 0x4d00
	s_addc_u32 s23, s95, 0
	s_add_u32 s24, s94, 0x4e00
	s_addc_u32 s25, s95, 0
	s_add_u32 s26, s94, 0x4f00
	s_addc_u32 s27, s95, 0
	s_add_u32 s28, s94, 0x5000
	s_addc_u32 s29, s95, 0
	s_add_u32 s30, s94, 0x5100
	s_addc_u32 s31, s95, 0
	s_add_u32 s34, s94, 0x5200
	s_addc_u32 s35, s95, 0
	s_add_u32 s36, s94, 0x5300
	s_addc_u32 s37, s95, 0
	s_mov_b32 s44, 1
	v_mov_b32_e32 v16, 0
	s_branch .LBB0_500

.LBB0_545:
	s_cmp_gt_i32 s6, 4
	s_cselect_b64 s[0:1], -1, 0
	s_cmp_lt_i32 s7, 5
	s_cselect_b64 s[2:3], -1, 0
	s_or_b64 s[0:1], s[0:1], s[2:3]
	s_and_b64 vcc, exec, s[0:1]
	s_cbranch_vccnz .LBB0_622
	s_mov_b32 s98, s88
	s_and_b32 s99, s88, 31
	s_lshl_b32 s99, s99, 3
	s_lshr_b32 s88, s88, 5
	s_or_b32 s88, s88, s99
	s_cmpk_gt_i32 s88, 0xff
	s_waitcnt vmcnt(0)
	v_mbcnt_lo_u32_b32 v0, -1, 0
	v_mbcnt_hi_u32_b32 v0, -1, v0
	v_mbcnt_lo_u32_b32 v9, -1, 0
	v_mbcnt_hi_u32_b32 v9, -1, v9
	s_cbranch_scc1 .LBB0_572
	s_ashr_i32 s28, s88, 31
	s_lshr_b32 s0, s28, 29
	s_add_i32 s3, s88, s0
	s_and_b32 s0, s3, -8
	s_sub_i32 s4, s88, s0
	s_cmp_gt_i32 s4, -1
	s_cbranch_scc0 .LBB0_549
	s_lshl_b32 s2, s4, 5
	s_cbranch_execz .LBB0_550
	s_branch .LBB0_551

.LBB0_572:
	v_readlane_b32 s6, v253, 23
	v_readlane_b32 s7, v253, 24
	s_mov_b32 s88, s98
	s_cmp_lt_u32 s7, 6
	s_cbranch_scc1 .LBB0_622
	v_readlane_b32 s0, v253, 20
	s_waitcnt vmcnt(0)
	s_lshl_b32 s0, s0, 6
	s_sub_i32 s0, 0, s0
	s_waitcnt vmcnt(0)
	s_barrier
	v_mbcnt_lo_u32_b32 v0, -1, 0
	v_mbcnt_hi_u32_b32 v0, -1, v0
	s_nop 0
	v_cmp_eq_u32_e32 vcc, s0, v0
	s_and_saveexec_b64 s[0:1], vcc
	s_cbranch_execz .LBB0_621
	s_add_i32 s2, 0, 0x20160
	v_mov_b32_e32 v0, s2
	s_waitcnt vmcnt(0) expcnt(0) lgkmcnt(0)
	ds_read_b32 v2, v0
	s_add_i32 s2, 0, 0x20164
	v_mov_b32_e32 v0, s2
	ds_read_b32 v0, v0
	s_waitcnt lgkmcnt(1)
	v_cmp_ne_u32_e32 vcc, 0, v2
	s_cbranch_vccnz .LBB0_589
	v_readlane_b32 s2, v253, 0
	v_readlane_b32 s3, v253, 1
	s_load_dwordx2 s[6:7], s[2:3], 0x4
	s_add_u32 s2, s94, 0x4200
	s_addc_u32 s3, s95, 0
	s_add_u32 s4, s94, 0x4400
	s_addc_u32 s5, s95, 0
	s_waitcnt lgkmcnt(0)
	s_mul_i32 s33, s6, s90
	s_add_u32 s6, s94, 0x4500
	s_mul_i32 s33, s33, s7
	s_addc_u32 s7, s95, 0
	s_add_u32 s8, s94, 0x4600
	s_addc_u32 s9, s95, 0
	s_add_u32 s10, s94, 0x4700
	s_addc_u32 s11, s95, 0
	s_add_u32 s12, s94, 0x4800
	s_addc_u32 s13, s95, 0
	s_add_u32 s14, s94, 0x4900
	s_addc_u32 s15, s95, 0
	s_add_u32 s16, s94, 0x4a00
	s_addc_u32 s17, s95, 0
	s_add_u32 s18, s94, 0x4b00
	s_addc_u32 s19, s95, 0
	s_add_u32 s20, s94, 0x4c00
	s_addc_u32 s21, s95, 0
	s_add_u32 s22, s94, 0x4d00
	s_addc_u32 s23, s95, 0
	s_add_u32 s24, s94, 0x4e00
	s_addc_u32 s25, s95, 0
	s_add_u32 s26, s94, 0x4f00
	s_addc_u32 s27, s95, 0
	s_add_u32 s28, s94, 0x5000
	s_addc_u32 s29, s95, 0
	s_add_u32 s30, s94, 0x5100
	s_addc_u32 s31, s95, 0
	s_add_u32 s34, s94, 0x5200
	s_addc_u32 s35, s95, 0
	s_add_u32 s36, s94, 0x5300
	s_addc_u32 s37, s95, 0
	s_mov_b32 s44, 1
	v_mov_b32_e32 v16, 0
	s_branch .LBB0_577

.LBB0_904:
	s_cmp_gt_i32 s6, 9
	s_cselect_b64 s[0:1], -1, 0
	s_cmp_lt_i32 s7, 10
	s_cselect_b64 s[2:3], -1, 0
	s_or_b64 s[0:1], s[0:1], s[2:3]
	s_and_b64 vcc, exec, s[0:1]
	s_cbranch_vccnz .LBB0_1038
	s_mov_b32 s98, s88
	s_and_b32 s99, s88, 31
	s_lshl_b32 s99, s99, 3
	s_lshr_b32 s88, s88, 5
	s_or_b32 s88, s88, s99
	s_waitcnt vmcnt(0)
	v_mov_b32_e32 v1, 0x420000
	v_mbcnt_lo_u32_b32 v0, -1, 0
	v_mbcnt_hi_u32_b32 v0, -1, v0
	global_load_dword v1, v1, s[94:95]
	s_and_b32 s0, s89, 0xffffffc0
	s_movk_i32 s1, 0x140
	v_add_u32_e32 v0, s0, v0
	s_add_u32 s2, s94, 0x420000
	s_addc_u32 s3, s95, 0
	v_cmp_gt_i32_e32 vcc, s1, v0
	s_waitcnt vmcnt(0)
	v_readfirstlane_b32 s41, v1
	s_and_saveexec_b64 s[0:1], vcc
	s_cbranch_execz .LBB0_907
	v_ashrrev_i32_e32 v1, 31, v0
	v_lshl_add_u64 v[2:3], v[0:1], 2, s[2:3]
	global_load_dword v1, v[2:3], off offset:4
	v_lshl_add_u32 v2, v0, 2, 0
	v_add_u32_e32 v2, 0x22400, v2
	s_waitcnt vmcnt(0)
	ds_write_b32 v2, v1

.LBB0_988:
	v_readlane_b32 s6, v253, 23
	v_readlane_b32 s7, v253, 24
	s_mov_b32 s88, s98
	s_cmp_lt_u32 s7, 11
	s_waitcnt vmcnt(0)
	s_barrier
	s_cbranch_scc1 .LBB0_1038
	v_readlane_b32 s0, v253, 20
	s_waitcnt vmcnt(0)
	s_lshl_b32 s0, s0, 6
	s_sub_i32 s0, 0, s0
	s_barrier
	v_mbcnt_lo_u32_b32 v0, -1, 0
	v_mbcnt_hi_u32_b32 v0, -1, v0
	s_nop 0
	v_cmp_eq_u32_e32 vcc, s0, v0
	s_and_saveexec_b64 s[0:1], vcc
	s_cbranch_execz .LBB0_1037
	s_add_i32 s2, 0, 0x20160
	v_mov_b32_e32 v0, s2
	s_waitcnt vmcnt(0) expcnt(0) lgkmcnt(0)
	ds_read_b32 v2, v0
	s_add_i32 s2, 0, 0x20164
	v_mov_b32_e32 v0, s2
	ds_read_b32 v0, v0
	s_waitcnt lgkmcnt(1)
	v_cmp_ne_u32_e32 vcc, 0, v2
	s_cbranch_vccnz .LBB0_1005
	v_readlane_b32 s2, v253, 0
	v_readlane_b32 s3, v253, 1
	s_load_dwordx2 s[6:7], s[2:3], 0x4
	s_add_u32 s2, s94, 0x4200
	s_addc_u32 s3, s95, 0
	s_add_u32 s4, s94, 0x4400
	s_addc_u32 s5, s95, 0
	s_waitcnt lgkmcnt(0)
	s_mul_i32 s33, s6, s90
	s_add_u32 s6, s94, 0x4500
	s_mul_i32 s33, s33, s7
	s_addc_u32 s7, s95, 0
	s_add_u32 s8, s94, 0x4600
	s_addc_u32 s9, s95, 0
	s_add_u32 s10, s94, 0x4700
	s_addc_u32 s11, s95, 0
	s_add_u32 s12, s94, 0x4800
	s_addc_u32 s13, s95, 0
	s_add_u32 s14, s94, 0x4900
	s_addc_u32 s15, s95, 0
	s_add_u32 s16, s94, 0x4a00
	s_addc_u32 s17, s95, 0
	s_add_u32 s18, s94, 0x4b00
	s_addc_u32 s19, s95, 0
	s_add_u32 s20, s94, 0x4c00
	s_addc_u32 s21, s95, 0
	s_add_u32 s22, s94, 0x4d00
	s_addc_u32 s23, s95, 0
	s_add_u32 s24, s94, 0x4e00
	s_addc_u32 s25, s95, 0
	s_add_u32 s26, s94, 0x4f00
	s_addc_u32 s27, s95, 0
	s_add_u32 s28, s94, 0x5000
	s_addc_u32 s29, s95, 0
	s_add_u32 s30, s94, 0x5100
	s_addc_u32 s31, s95, 0
	s_add_u32 s34, s94, 0x5200
	s_addc_u32 s35, s95, 0
	s_add_u32 s36, s94, 0x5300
	s_addc_u32 s37, s95, 0
	s_mov_b32 s44, 1
	v_mov_b32_e32 v16, 0
	s_branch .LBB0_993

.LBB0_1038:
	s_cmp_gt_i32 s6, 10
	s_cselect_b64 s[0:1], -1, 0
	s_cmp_lt_i32 s7, 11
	s_cselect_b64 s[2:3], -1, 0
	s_or_b64 s[0:1], s[0:1], s[2:3]
	s_and_b64 vcc, exec, s[0:1]
	s_cbranch_vccnz .LBB0_1136
	s_mov_b32 s98, s88
	s_and_b32 s99, s88, 31
	s_lshl_b32 s99, s99, 3
	s_lshr_b32 s88, s88, 5
	s_or_b32 s88, s88, s99
	s_waitcnt vmcnt(0)
	v_mov_b32_e32 v1, 0x420000
	v_mbcnt_lo_u32_b32 v0, -1, 0
	v_mbcnt_hi_u32_b32 v0, -1, v0
	global_load_dword v1, v1, s[94:95]
	s_and_b32 s0, s89, 0xffffffc0
	s_movk_i32 s1, 0x140
	v_add_u32_e32 v0, s0, v0
	s_add_u32 s2, s94, 0x420000
	s_addc_u32 s3, s95, 0
	v_cmp_gt_i32_e32 vcc, s1, v0
	s_waitcnt vmcnt(0)
	v_readfirstlane_b32 s44, v1
	s_and_saveexec_b64 s[0:1], vcc
	s_cbranch_execz .LBB0_1041
	v_ashrrev_i32_e32 v1, 31, v0
	v_lshl_add_u64 v[2:3], v[0:1], 2, s[2:3]
	global_load_dword v1, v[2:3], off offset:4
	v_lshl_add_u32 v0, v0, 2, 0
	v_add_u32_e32 v0, 0x22400, v0
	s_waitcnt vmcnt(0)
	ds_write_b32 v0, v1

.LBB0_1086:
	v_readlane_b32 s6, v253, 23
	v_readlane_b32 s7, v253, 24
	s_mov_b32 s88, s98
	s_cmp_lt_u32 s7, 12
	s_waitcnt vmcnt(0)
	s_barrier
	s_cbranch_scc1 .LBB0_1136
	v_readlane_b32 s0, v253, 20
	s_waitcnt vmcnt(0)
	s_lshl_b32 s0, s0, 6
	s_sub_i32 s0, 0, s0
	s_barrier
	v_mbcnt_lo_u32_b32 v0, -1, 0
	v_mbcnt_hi_u32_b32 v0, -1, v0
	s_nop 0
	v_cmp_eq_u32_e32 vcc, s0, v0
	s_and_saveexec_b64 s[0:1], vcc
	s_cbranch_execz .LBB0_1135
	s_add_i32 s2, 0, 0x20160
	v_mov_b32_e32 v0, s2
	s_waitcnt vmcnt(0) expcnt(0) lgkmcnt(0)
	ds_read_b32 v2, v0
	s_add_i32 s2, 0, 0x20164
	v_mov_b32_e32 v0, s2
	ds_read_b32 v0, v0
	s_waitcnt lgkmcnt(1)
	v_cmp_ne_u32_e32 vcc, 0, v2
	s_cbranch_vccnz .LBB0_1103
	v_readlane_b32 s2, v253, 0
	v_readlane_b32 s3, v253, 1
	s_load_dwordx2 s[6:7], s[2:3], 0x4
	s_add_u32 s2, s94, 0x4200
	s_addc_u32 s3, s95, 0
	s_add_u32 s4, s94, 0x4400
	s_addc_u32 s5, s95, 0
	s_waitcnt lgkmcnt(0)
	s_mul_i32 s33, s6, s90
	s_add_u32 s6, s94, 0x4500
	s_mul_i32 s33, s33, s7
	s_addc_u32 s7, s95, 0
	s_add_u32 s8, s94, 0x4600
	s_addc_u32 s9, s95, 0
	s_add_u32 s10, s94, 0x4700
	s_addc_u32 s11, s95, 0
	s_add_u32 s12, s94, 0x4800
	s_addc_u32 s13, s95, 0
	s_add_u32 s14, s94, 0x4900
	s_addc_u32 s15, s95, 0
	s_add_u32 s16, s94, 0x4a00
	s_addc_u32 s17, s95, 0
	s_add_u32 s18, s94, 0x4b00
	s_addc_u32 s19, s95, 0
	s_add_u32 s20, s94, 0x4c00
	s_addc_u32 s21, s95, 0
	s_add_u32 s22, s94, 0x4d00
	s_addc_u32 s23, s95, 0
	s_add_u32 s24, s94, 0x4e00
	s_addc_u32 s25, s95, 0
	s_add_u32 s26, s94, 0x4f00
	s_addc_u32 s27, s95, 0
	s_add_u32 s28, s94, 0x5000
	s_addc_u32 s29, s95, 0
	s_add_u32 s30, s94, 0x5100
	s_addc_u32 s31, s95, 0
	s_add_u32 s34, s94, 0x5200
	s_addc_u32 s35, s95, 0
	s_add_u32 s36, s94, 0x5300
	s_addc_u32 s37, s95, 0
	s_mov_b32 s44, 1
	v_mov_b32_e32 v16, 0
	s_branch .LBB0_1091

.LBB0_1212:
	s_cmp_gt_i32 s6, 18
	s_cselect_b64 s[0:1], -1, 0
	s_cmp_lt_i32 s7, 19
	s_cselect_b64 s[2:3], -1, 0
	s_or_b64 s[0:1], s[0:1], s[2:3]
	s_and_b64 vcc, exec, s[0:1]
	s_cbranch_vccnz .LBB0_1297
	s_mov_b32 s98, s88
	s_and_b32 s99, s88, 31
	s_lshl_b32 s99, s99, 3
	s_lshr_b32 s88, s88, 5
	s_or_b32 s88, s88, s99
	s_and_b32 s0, s89, 0xffffffc0
	s_waitcnt vmcnt(0)
	v_mbcnt_lo_u32_b32 v0, -1, 0
	v_mbcnt_hi_u32_b32 v0, -1, v0
	s_nop 0
	v_add_u32_e32 v2, s0, v0
	s_movk_i32 s0, 0x800
	v_cmp_gt_i32_e32 vcc, s0, v2
	s_and_saveexec_b64 s[6:7], vcc
	s_cbranch_execz .LBB0_1220
	v_readlane_b32 s1, v253, 20
	s_lshl_b32 s0, s1, 8
	s_add_i32 s0, s0, 0
	v_lshl_add_u32 v1, v0, 2, s0
	v_lshlrev_b32_e32 v0, 1, v0
	v_add_u32_e32 v3, 0x20400, v1
	v_lshl_add_u32 v4, s1, 7, v0
	s_mov_b64 s[8:9], 0
	v_mov_b32_e32 v5, 0x461c4000
	s_mov_b32 s12, 0x3f2aaaab
	v_mov_b32_e32 v6, 0x3e91f4c4
	s_mov_b32 s13, 0x3f317218
	s_movk_i32 s14, 0x204
	s_mov_b32 s15, 0x7f800000
	s_mov_b32 s16, 0x42b17218
	v_mov_b32_e32 v7, 0x37000000
	s_mov_b32 s17, 0x3fb8aa3b
	s_mov_b32 s18, 0xc2ce8ed0
	v_mov_b32_e32 v8, 0x7f800000
	s_brev_b32 s19, 18
	s_mov_b32 s20, 0xfe5163ab
	v_mov_b32_e32 v1, 0
	s_mov_b32 s21, 0x3c439041
	s_mov_b32 s22, 0xdb629599
	s_mov_b32 s23, 0xf534ddc0
	s_mov_b32 s24, 0xfc2757d1
	s_mov_b32 s25, 0x4e441529
	s_mov_b32 s26, 0xa2f9836e
	s_mov_b32 s27, 0x3fc90fda
	s_mov_b32 s28, 0x3f22f983
	s_mov_b32 s29, 0xbfc90fda
	v_mov_b32_e32 v9, 0x3c0881c4
	v_mov_b32_e32 v10, 0xbab64f3b
	s_brev_b32 s30, 1
	s_movk_i32 s31, 0x1f8
	s_movk_i32 s33, 0x5ff
	v_not_b32_e32 v11, 63
	v_not_b32_e32 v12, 31
	v_mov_b32_e32 v13, 0x7fc00000
	s_branch .LBB0_1216

.LBB0_1247:
	v_readlane_b32 s6, v253, 23
	v_readlane_b32 s7, v253, 24
	s_mov_b32 s88, s98
	s_cmp_gt_u32 s7, 19
	s_cbranch_scc0 .LBB0_1297
	v_readlane_b32 s0, v253, 20
	s_waitcnt vmcnt(0)
	s_lshl_b32 s0, s0, 6
	s_sub_i32 s0, 0, s0
	s_waitcnt vmcnt(0)
	s_barrier
	v_mbcnt_lo_u32_b32 v0, -1, 0
	v_mbcnt_hi_u32_b32 v0, -1, v0
	s_nop 0
	v_cmp_eq_u32_e32 vcc, s0, v0
	s_and_saveexec_b64 s[0:1], vcc
	s_cbranch_execz .LBB0_1296
	s_add_i32 s2, 0, 0x20160
	v_mov_b32_e32 v0, s2
	s_waitcnt vmcnt(0) expcnt(0) lgkmcnt(0)
	ds_read_b32 v2, v0
	s_add_i32 s2, 0, 0x20164
	v_mov_b32_e32 v0, s2
	ds_read_b32 v0, v0
	s_waitcnt lgkmcnt(1)
	v_cmp_ne_u32_e32 vcc, 0, v2
	s_cbranch_vccnz .LBB0_1264
	v_readlane_b32 s2, v253, 0
	v_readlane_b32 s3, v253, 1
	s_load_dwordx2 s[6:7], s[2:3], 0x4
	s_add_u32 s2, s94, 0x4200
	s_addc_u32 s3, s95, 0
	s_add_u32 s4, s94, 0x4400
	s_addc_u32 s5, s95, 0
	s_waitcnt lgkmcnt(0)
	s_mul_i32 s33, s6, s90
	s_add_u32 s6, s94, 0x4500
	s_mul_i32 s33, s33, s7
	s_addc_u32 s7, s95, 0
	s_add_u32 s8, s94, 0x4600
	s_addc_u32 s9, s95, 0
	s_add_u32 s10, s94, 0x4700
	s_addc_u32 s11, s95, 0
	s_add_u32 s12, s94, 0x4800
	s_addc_u32 s13, s95, 0
	s_add_u32 s14, s94, 0x4900
	s_addc_u32 s15, s95, 0
	s_add_u32 s16, s94, 0x4a00
	s_addc_u32 s17, s95, 0
	s_add_u32 s18, s94, 0x4b00
	s_addc_u32 s19, s95, 0
	s_add_u32 s20, s94, 0x4c00
	s_addc_u32 s21, s95, 0
	s_add_u32 s22, s94, 0x4d00
	s_addc_u32 s23, s95, 0
	s_add_u32 s24, s94, 0x4e00
	s_addc_u32 s25, s95, 0
	s_add_u32 s26, s94, 0x4f00
	s_addc_u32 s27, s95, 0
	s_add_u32 s28, s94, 0x5000
	s_addc_u32 s29, s95, 0
	s_add_u32 s30, s94, 0x5100
	s_addc_u32 s31, s95, 0
	s_add_u32 s34, s94, 0x5200
	s_addc_u32 s35, s95, 0
	s_add_u32 s36, s94, 0x5300
	s_addc_u32 s37, s95, 0
	s_mov_b32 s44, 1
	v_mov_b32_e32 v16, 0
	s_branch .LBB0_1252

.LBB0_1370:
	s_cmp_gt_i32 s6, 21
	s_cselect_b64 s[0:1], -1, 0
	s_cmp_lt_i32 s7, 22
	s_cselect_b64 s[2:3], -1, 0
	s_or_b64 s[0:1], s[0:1], s[2:3]
	s_and_b64 vcc, exec, s[0:1]
	s_cbranch_vccnz .LBB0_1445
	s_mov_b32 s98, s88
	s_and_b32 s99, s88, 31
	s_lshl_b32 s99, s99, 3
	s_lshr_b32 s88, s88, 5
	s_or_b32 s88, s88, s99
	s_cmpk_gt_i32 s88, 0xff
	s_waitcnt vmcnt(0)
	v_mbcnt_lo_u32_b32 v0, -1, 0
	v_mbcnt_hi_u32_b32 v0, -1, v0
	v_mbcnt_lo_u32_b32 v8, -1, 0
	v_mbcnt_hi_u32_b32 v8, -1, v8
	s_cbranch_scc1 .LBB0_1395
	s_ashr_i32 s28, s88, 31
	s_lshr_b32 s0, s28, 29
	s_add_i32 s3, s88, s0
	s_and_b32 s0, s3, -8
	s_sub_i32 s4, s88, s0
	s_cmp_gt_i32 s4, -1
	s_cbranch_scc0 .LBB0_1374
	s_lshl_b32 s2, s4, 5
	s_cbranch_execz .LBB0_1375
	s_branch .LBB0_1376

.LBB0_1395:
	v_readlane_b32 s6, v253, 23
	v_readlane_b32 s7, v253, 24
	s_mov_b32 s88, s98
	s_cmp_lt_u32 s7, 23
	s_cbranch_scc1 .LBB0_1445
	v_readlane_b32 s0, v253, 20
	s_waitcnt vmcnt(0)
	s_lshl_b32 s0, s0, 6
	s_sub_i32 s0, 0, s0
	s_waitcnt vmcnt(0)
	s_barrier
	v_mbcnt_lo_u32_b32 v0, -1, 0
	v_mbcnt_hi_u32_b32 v0, -1, v0
	s_nop 0
	v_cmp_eq_u32_e32 vcc, s0, v0
	s_and_saveexec_b64 s[0:1], vcc
	s_cbranch_execz .LBB0_1444
	s_add_i32 s2, 0, 0x20160
	v_mov_b32_e32 v0, s2
	s_waitcnt vmcnt(0) expcnt(0) lgkmcnt(0)
	ds_read_b32 v2, v0
	s_add_i32 s2, 0, 0x20164
	v_mov_b32_e32 v0, s2
	ds_read_b32 v0, v0
	s_waitcnt lgkmcnt(1)
	v_cmp_ne_u32_e32 vcc, 0, v2
	s_cbranch_vccnz .LBB0_1412
	v_readlane_b32 s2, v253, 0
	v_readlane_b32 s3, v253, 1
	s_load_dwordx2 s[6:7], s[2:3], 0x4
	s_add_u32 s2, s94, 0x4200
	s_addc_u32 s3, s95, 0
	s_add_u32 s4, s94, 0x4400
	s_addc_u32 s5, s95, 0
	s_waitcnt lgkmcnt(0)
	s_mul_i32 s33, s6, s90
	s_add_u32 s6, s94, 0x4500
	s_mul_i32 s33, s33, s7
	s_addc_u32 s7, s95, 0
	s_add_u32 s8, s94, 0x4600
	s_addc_u32 s9, s95, 0
	s_add_u32 s10, s94, 0x4700
	s_addc_u32 s11, s95, 0
	s_add_u32 s12, s94, 0x4800
	s_addc_u32 s13, s95, 0
	s_add_u32 s14, s94, 0x4900
	s_addc_u32 s15, s95, 0
	s_add_u32 s16, s94, 0x4a00
	s_addc_u32 s17, s95, 0
	s_add_u32 s18, s94, 0x4b00
	s_addc_u32 s19, s95, 0
	s_add_u32 s20, s94, 0x4c00
	s_addc_u32 s21, s95, 0
	s_add_u32 s22, s94, 0x4d00
	s_addc_u32 s23, s95, 0
	s_add_u32 s24, s94, 0x4e00
	s_addc_u32 s25, s95, 0
	s_add_u32 s26, s94, 0x4f00
	s_addc_u32 s27, s95, 0
	s_add_u32 s28, s94, 0x5000
	s_addc_u32 s29, s95, 0
	s_add_u32 s30, s94, 0x5100
	s_addc_u32 s31, s95, 0
	s_add_u32 s34, s94, 0x5200
	s_addc_u32 s35, s95, 0
	s_add_u32 s36, s94, 0x5300
	s_addc_u32 s37, s95, 0
	s_mov_b32 s44, 1
	v_mov_b32_e32 v16, 0
	s_branch .LBB0_1400

.LBB0_1727:
	s_cmp_gt_i32 s6, 25
	s_cselect_b64 s[0:1], -1, 0
	s_cmp_lt_i32 s7, 26
	s_cselect_b64 s[2:3], -1, 0
	s_or_b64 s[0:1], s[0:1], s[2:3]
	s_and_b64 vcc, exec, s[0:1]
	s_cbranch_vccnz .LBB0_1861
	s_mov_b32 s98, s88
	s_and_b32 s99, s88, 31
	s_lshl_b32 s99, s99, 3
	s_lshr_b32 s88, s88, 5
	s_or_b32 s88, s88, s99
	s_waitcnt vmcnt(0)
	v_mov_b32_e32 v1, 0x420000
	v_mbcnt_lo_u32_b32 v0, -1, 0
	v_mbcnt_hi_u32_b32 v0, -1, v0
	global_load_dword v1, v1, s[94:95]
	s_and_b32 s0, s89, 0xffffffc0
	s_movk_i32 s1, 0x140
	v_add_u32_e32 v0, s0, v0
	s_add_u32 s2, s94, 0x420000
	s_addc_u32 s3, s95, 0
	v_cmp_gt_i32_e32 vcc, s1, v0
	s_waitcnt vmcnt(0)
	v_readfirstlane_b32 s41, v1
	s_and_saveexec_b64 s[0:1], vcc
	s_cbranch_execz .LBB0_1730
	v_ashrrev_i32_e32 v1, 31, v0
	v_lshl_add_u64 v[2:3], v[0:1], 2, s[2:3]
	global_load_dword v1, v[2:3], off offset:4
	v_lshl_add_u32 v2, v0, 2, 0
	v_add_u32_e32 v2, 0x22400, v2
	s_waitcnt vmcnt(0)
	ds_write_b32 v2, v1

.LBB0_1811:
	v_readlane_b32 s6, v253, 23
	v_readlane_b32 s7, v253, 24
	s_mov_b32 s88, s98
	s_cmp_lt_u32 s7, 27
	s_waitcnt vmcnt(0)
	s_barrier
	s_cbranch_scc1 .LBB0_1861
	v_readlane_b32 s0, v253, 20
	s_waitcnt vmcnt(0)
	s_lshl_b32 s0, s0, 6
	s_sub_i32 s0, 0, s0
	s_barrier
	v_mbcnt_lo_u32_b32 v0, -1, 0
	v_mbcnt_hi_u32_b32 v0, -1, v0
	s_nop 0
	v_cmp_eq_u32_e32 vcc, s0, v0
	s_and_saveexec_b64 s[0:1], vcc
	s_cbranch_execz .LBB0_1860
	s_add_i32 s2, 0, 0x20160
	v_mov_b32_e32 v0, s2
	s_waitcnt vmcnt(0) expcnt(0) lgkmcnt(0)
	ds_read_b32 v2, v0
	s_add_i32 s2, 0, 0x20164
	v_mov_b32_e32 v0, s2
	ds_read_b32 v0, v0
	s_waitcnt lgkmcnt(1)
	v_cmp_ne_u32_e32 vcc, 0, v2
	s_cbranch_vccnz .LBB0_1828
	v_readlane_b32 s2, v253, 0
	v_readlane_b32 s3, v253, 1
	s_load_dwordx2 s[6:7], s[2:3], 0x4
	s_add_u32 s2, s94, 0x4200
	s_addc_u32 s3, s95, 0
	s_add_u32 s4, s94, 0x4400
	s_addc_u32 s5, s95, 0
	s_waitcnt lgkmcnt(0)
	s_mul_i32 s33, s6, s90
	s_add_u32 s6, s94, 0x4500
	s_mul_i32 s33, s33, s7
	s_addc_u32 s7, s95, 0
	s_add_u32 s8, s94, 0x4600
	s_addc_u32 s9, s95, 0
	s_add_u32 s10, s94, 0x4700
	s_addc_u32 s11, s95, 0
	s_add_u32 s12, s94, 0x4800
	s_addc_u32 s13, s95, 0
	s_add_u32 s14, s94, 0x4900
	s_addc_u32 s15, s95, 0
	s_add_u32 s16, s94, 0x4a00
	s_addc_u32 s17, s95, 0
	s_add_u32 s18, s94, 0x4b00
	s_addc_u32 s19, s95, 0
	s_add_u32 s20, s94, 0x4c00
	s_addc_u32 s21, s95, 0
	s_add_u32 s22, s94, 0x4d00
	s_addc_u32 s23, s95, 0
	s_add_u32 s24, s94, 0x4e00
	s_addc_u32 s25, s95, 0
	s_add_u32 s26, s94, 0x4f00
	s_addc_u32 s27, s95, 0
	s_add_u32 s28, s94, 0x5000
	s_addc_u32 s29, s95, 0
	s_add_u32 s30, s94, 0x5100
	s_addc_u32 s31, s95, 0
	s_add_u32 s34, s94, 0x5200
	s_addc_u32 s35, s95, 0
	s_add_u32 s36, s94, 0x5300
	s_addc_u32 s37, s95, 0
	s_mov_b32 s44, 1
	v_mov_b32_e32 v16, 0
	s_branch .LBB0_1816

.LBB0_1861:
	s_cmp_gt_i32 s6, 26
	s_cselect_b64 s[0:1], -1, 0
	s_cmp_lt_i32 s7, 27
	s_cselect_b64 s[2:3], -1, 0
	s_or_b64 s[0:1], s[0:1], s[2:3]
	s_and_b64 vcc, exec, s[0:1]
	s_cbranch_vccnz .LBB0_1959
	s_mov_b32 s98, s88
	s_and_b32 s99, s88, 31
	s_lshl_b32 s99, s99, 3
	s_lshr_b32 s88, s88, 5
	s_or_b32 s88, s88, s99
	s_waitcnt vmcnt(0)
	v_mov_b32_e32 v1, 0x420000
	v_mbcnt_lo_u32_b32 v0, -1, 0
	v_mbcnt_hi_u32_b32 v0, -1, v0
	global_load_dword v1, v1, s[94:95]
	s_and_b32 s0, s89, 0xffffffc0
	s_movk_i32 s1, 0x140
	v_add_u32_e32 v0, s0, v0
	s_add_u32 s2, s94, 0x420000
	s_addc_u32 s3, s95, 0
	v_cmp_gt_i32_e32 vcc, s1, v0
	s_waitcnt vmcnt(0)
	v_readfirstlane_b32 s44, v1
	s_and_saveexec_b64 s[0:1], vcc
	s_cbranch_execz .LBB0_1864
	v_ashrrev_i32_e32 v1, 31, v0
	v_lshl_add_u64 v[2:3], v[0:1], 2, s[2:3]
	global_load_dword v1, v[2:3], off offset:4
	v_lshl_add_u32 v0, v0, 2, 0
	v_add_u32_e32 v0, 0x22400, v0
	s_waitcnt vmcnt(0)
	ds_write_b32 v0, v1

.LBB0_1909:
	v_readlane_b32 s6, v253, 23
	v_readlane_b32 s7, v253, 24
	s_mov_b32 s88, s98
	s_cmp_lt_u32 s7, 28
	s_waitcnt vmcnt(0)
	s_barrier
	s_cbranch_scc1 .LBB0_1959
	v_readlane_b32 s0, v253, 20
	s_waitcnt vmcnt(0)
	s_lshl_b32 s0, s0, 6
	s_sub_i32 s0, 0, s0
	s_barrier
	v_mbcnt_lo_u32_b32 v0, -1, 0
	v_mbcnt_hi_u32_b32 v0, -1, v0
	s_nop 0
	v_cmp_eq_u32_e32 vcc, s0, v0
	s_and_saveexec_b64 s[0:1], vcc
	s_cbranch_execz .LBB0_1958
	s_add_i32 s2, 0, 0x20160
	v_mov_b32_e32 v0, s2
	s_waitcnt vmcnt(0) expcnt(0) lgkmcnt(0)
	ds_read_b32 v2, v0
	s_add_i32 s2, 0, 0x20164
	v_mov_b32_e32 v0, s2
	ds_read_b32 v0, v0
	s_waitcnt lgkmcnt(1)
	v_cmp_ne_u32_e32 vcc, 0, v2
	s_cbranch_vccnz .LBB0_1926
	v_readlane_b32 s2, v253, 0
	v_readlane_b32 s3, v253, 1
	s_load_dwordx2 s[6:7], s[2:3], 0x4
	s_add_u32 s2, s94, 0x4200
	s_addc_u32 s3, s95, 0
	s_add_u32 s4, s94, 0x4400
	s_addc_u32 s5, s95, 0
	s_waitcnt lgkmcnt(0)
	s_mul_i32 s33, s6, s90
	s_add_u32 s6, s94, 0x4500
	s_mul_i32 s33, s33, s7
	s_addc_u32 s7, s95, 0
	s_add_u32 s8, s94, 0x4600
	s_addc_u32 s9, s95, 0
	s_add_u32 s10, s94, 0x4700
	s_addc_u32 s11, s95, 0
	s_add_u32 s12, s94, 0x4800
	s_addc_u32 s13, s95, 0
	s_add_u32 s14, s94, 0x4900
	s_addc_u32 s15, s95, 0
	s_add_u32 s16, s94, 0x4a00
	s_addc_u32 s17, s95, 0
	s_add_u32 s18, s94, 0x4b00
	s_addc_u32 s19, s95, 0
	s_add_u32 s20, s94, 0x4c00
	s_addc_u32 s21, s95, 0
	s_add_u32 s22, s94, 0x4d00
	s_addc_u32 s23, s95, 0
	s_add_u32 s24, s94, 0x4e00
	s_addc_u32 s25, s95, 0
	s_add_u32 s26, s94, 0x4f00
	s_addc_u32 s27, s95, 0
	s_add_u32 s28, s94, 0x5000
	s_addc_u32 s29, s95, 0
	s_add_u32 s30, s94, 0x5100
	s_addc_u32 s31, s95, 0
	s_add_u32 s34, s94, 0x5200
	s_addc_u32 s35, s95, 0
	s_add_u32 s36, s94, 0x5300
	s_addc_u32 s37, s95, 0
	s_mov_b32 s44, 1
	v_mov_b32_e32 v16, 0
	s_branch .LBB0_1914

.LBB0_2038:
	s_cmp_gt_i32 s6, 34
	s_cselect_b64 s[0:1], -1, 0
	s_cmp_lt_i32 s7, 35
	s_cselect_b64 s[2:3], -1, 0
	s_or_b64 s[0:1], s[0:1], s[2:3]
	s_and_b64 vcc, exec, s[0:1]
	s_cbranch_vccnz .LBB0_2128
	s_mov_b32 s98, s88
	s_and_b32 s99, s88, 31
	s_lshl_b32 s99, s99, 3
	s_lshr_b32 s88, s88, 5
	s_or_b32 s88, s88, s99
	s_add_u32 s6, s94, 0x4a600000
	s_addc_u32 s7, s95, 0
	s_cmpk_lt_i32 s88, 0x100
	v_mbcnt_lo_u32_b32 v144, -1, 0
	v_mbcnt_hi_u32_b32 v144, -1, v144
	s_waitcnt vmcnt(0)
	v_mbcnt_lo_u32_b32 v8, -1, 0
	v_mbcnt_hi_u32_b32 v8, -1, v8
	s_cbranch_scc1 .LBB0_2041
	s_ashr_i32 s43, s90, 31
	s_mov_b32 s42, 0
	s_cbranch_execz .LBB0_2042
	s_branch .LBB0_2065

.LBB0_2078:
	v_readlane_b32 s6, v253, 23
	v_readlane_b32 s7, v253, 24
	s_mov_b32 s88, s98
	s_cmp_gt_u32 s7, 35
	s_cbranch_scc0 .LBB0_2128
	v_readlane_b32 s0, v253, 20
	s_waitcnt vmcnt(0)
	s_lshl_b32 s0, s0, 6
	s_sub_i32 s0, 0, s0
	s_waitcnt vmcnt(63) expcnt(7) lgkmcnt(15)
	s_barrier
	v_mbcnt_lo_u32_b32 v0, -1, 0
	v_mbcnt_hi_u32_b32 v0, -1, v0
	s_nop 0
	v_cmp_eq_u32_e32 vcc, s0, v0
	s_and_saveexec_b64 s[0:1], vcc
	s_cbranch_execz .LBB0_2127
	s_add_i32 s2, 0, 0x20160
	v_mov_b32_e32 v0, s2
	s_waitcnt vmcnt(0) expcnt(0) lgkmcnt(0)
	ds_read_b32 v2, v0
	s_add_i32 s2, 0, 0x20164
	v_mov_b32_e32 v0, s2
	ds_read_b32 v0, v0
	s_waitcnt lgkmcnt(1)
	v_cmp_ne_u32_e32 vcc, 0, v2
	s_cbranch_vccnz .LBB0_2095
	v_readlane_b32 s2, v253, 0
	v_readlane_b32 s3, v253, 1
	s_load_dwordx2 s[6:7], s[2:3], 0x4
	s_add_u32 s2, s94, 0x4200
	s_addc_u32 s3, s95, 0
	s_add_u32 s4, s94, 0x4400
	s_addc_u32 s5, s95, 0
	s_waitcnt lgkmcnt(0)
	s_mul_i32 s33, s6, s90
	s_add_u32 s6, s94, 0x4500
	s_mul_i32 s33, s33, s7
	s_addc_u32 s7, s95, 0
	s_add_u32 s8, s94, 0x4600
	s_addc_u32 s9, s95, 0
	s_add_u32 s10, s94, 0x4700
	s_addc_u32 s11, s95, 0
	s_add_u32 s12, s94, 0x4800
	s_addc_u32 s13, s95, 0
	s_add_u32 s14, s94, 0x4900
	s_addc_u32 s15, s95, 0
	s_add_u32 s16, s94, 0x4a00
	s_addc_u32 s17, s95, 0
	s_add_u32 s18, s94, 0x4b00
	s_addc_u32 s19, s95, 0
	s_add_u32 s20, s94, 0x4c00
	s_addc_u32 s21, s95, 0
	s_add_u32 s22, s94, 0x4d00
	s_addc_u32 s23, s95, 0
	s_add_u32 s24, s94, 0x4e00
	s_addc_u32 s25, s95, 0
	s_add_u32 s26, s94, 0x4f00
	s_addc_u32 s27, s95, 0
	s_add_u32 s28, s94, 0x5000
	s_addc_u32 s29, s95, 0
	s_add_u32 s30, s94, 0x5100
	s_addc_u32 s31, s95, 0
	s_add_u32 s34, s94, 0x5200
	s_addc_u32 s35, s95, 0
	s_add_u32 s36, s94, 0x5300
	s_addc_u32 s37, s95, 0
	s_mov_b32 s44, 1
	v_mov_b32_e32 v16, 0
	s_branch .LBB0_2083

.LBB0_2128:
	s_cmp_gt_i32 s6, 36
	s_cselect_b64 s[0:1], -1, 0
	s_cmp_lt_i32 s7, 37
	s_cselect_b64 s[2:3], -1, 0
	s_or_b64 s[0:1], s[0:1], s[2:3]
	s_and_b64 vcc, exec, s[0:1]
	s_cbranch_vccnz .LBB0_2203
	s_mov_b32 s98, s88
	s_and_b32 s99, s88, 31
	s_lshl_b32 s99, s99, 3
	s_lshr_b32 s88, s88, 5
	s_or_b32 s88, s88, s99
	s_cmpk_gt_i32 s88, 0xff
	s_waitcnt vmcnt(0)
	v_mbcnt_lo_u32_b32 v0, -1, 0
	v_mbcnt_hi_u32_b32 v0, -1, v0
	v_mbcnt_lo_u32_b32 v8, -1, 0
	v_mbcnt_hi_u32_b32 v8, -1, v8
	s_cbranch_scc1 .LBB0_2153
	s_ashr_i32 s28, s88, 31
	s_lshr_b32 s0, s28, 29
	s_add_i32 s3, s88, s0
	s_and_b32 s0, s3, -8
	s_sub_i32 s4, s88, s0
	s_cmp_gt_i32 s4, -1
	s_cbranch_scc0 .LBB0_2132
	s_lshl_b32 s2, s4, 5
	s_cbranch_execz .LBB0_2133
	s_branch .LBB0_2134

.LBB0_2153:
	v_readlane_b32 s6, v253, 23
	v_readlane_b32 s7, v253, 24
	s_mov_b32 s88, s98
	s_cmp_lt_u32 s7, 38
	s_cbranch_scc1 .LBB0_2203
	v_readlane_b32 s0, v253, 20
	s_waitcnt vmcnt(0)
	s_lshl_b32 s0, s0, 6
	s_sub_i32 s0, 0, s0
	s_waitcnt vmcnt(0)
	s_barrier
	v_mbcnt_lo_u32_b32 v0, -1, 0
	v_mbcnt_hi_u32_b32 v0, -1, v0
	s_nop 0
	v_cmp_eq_u32_e32 vcc, s0, v0
	s_and_saveexec_b64 s[0:1], vcc
	s_cbranch_execz .LBB0_2202
	s_add_i32 s2, 0, 0x20160
	v_mov_b32_e32 v0, s2
	s_waitcnt vmcnt(0) expcnt(0) lgkmcnt(0)
	ds_read_b32 v2, v0
	s_add_i32 s2, 0, 0x20164
	v_mov_b32_e32 v0, s2
	ds_read_b32 v0, v0
	s_waitcnt lgkmcnt(1)
	v_cmp_ne_u32_e32 vcc, 0, v2
	s_cbranch_vccnz .LBB0_2170
	v_readlane_b32 s2, v253, 0
	v_readlane_b32 s3, v253, 1
	s_load_dwordx2 s[6:7], s[2:3], 0x4
	s_add_u32 s2, s94, 0x4200
	s_addc_u32 s3, s95, 0
	s_add_u32 s4, s94, 0x4400
	s_addc_u32 s5, s95, 0
	s_waitcnt lgkmcnt(0)
	s_mul_i32 s33, s6, s90
	s_add_u32 s6, s94, 0x4500
	s_mul_i32 s33, s33, s7
	s_addc_u32 s7, s95, 0
	s_add_u32 s8, s94, 0x4600
	s_addc_u32 s9, s95, 0
	s_add_u32 s10, s94, 0x4700
	s_addc_u32 s11, s95, 0
	s_add_u32 s12, s94, 0x4800
	s_addc_u32 s13, s95, 0
	s_add_u32 s14, s94, 0x4900
	s_addc_u32 s15, s95, 0
	s_add_u32 s16, s94, 0x4a00
	s_addc_u32 s17, s95, 0
	s_add_u32 s18, s94, 0x4b00
	s_addc_u32 s19, s95, 0
	s_add_u32 s20, s94, 0x4c00
	s_addc_u32 s21, s95, 0
	s_add_u32 s22, s94, 0x4d00
	s_addc_u32 s23, s95, 0
	s_add_u32 s24, s94, 0x4e00
	s_addc_u32 s25, s95, 0
	s_add_u32 s26, s94, 0x4f00
	s_addc_u32 s27, s95, 0
	s_add_u32 s28, s94, 0x5000
	s_addc_u32 s29, s95, 0
	s_add_u32 s30, s94, 0x5100
	s_addc_u32 s31, s95, 0
	s_add_u32 s34, s94, 0x5200
	s_addc_u32 s35, s95, 0
	s_add_u32 s36, s94, 0x5300
	s_addc_u32 s37, s95, 0
	s_mov_b32 s44, 1
	v_mov_b32_e32 v16, 0
	s_branch .LBB0_2158

.LBB0_2203:
	s_cmp_gt_i32 s6, 37
	s_cselect_b64 s[0:1], -1, 0
	s_cmp_lt_i32 s7, 38
	s_cselect_b64 s[2:3], -1, 0
	s_or_b64 s[0:1], s[0:1], s[2:3]
	s_and_b64 vcc, exec, s[0:1]
	s_cbranch_vccnz .LBB0_2278
	s_mov_b32 s98, s88
	s_and_b32 s99, s88, 31
	s_lshl_b32 s99, s99, 3
	s_lshr_b32 s88, s88, 5
	s_or_b32 s88, s88, s99
	s_cmpk_gt_i32 s88, 0xff
	s_waitcnt vmcnt(0)
	v_mbcnt_lo_u32_b32 v0, -1, 0
	v_mbcnt_hi_u32_b32 v0, -1, v0
	v_mbcnt_lo_u32_b32 v8, -1, 0
	v_mbcnt_hi_u32_b32 v8, -1, v8
	s_cbranch_scc1 .LBB0_2228
	s_ashr_i32 s30, s88, 31
	s_lshr_b32 s0, s30, 29
	s_add_i32 s2, s88, s0
	s_and_b32 s0, s2, -8
	s_sub_i32 s3, s88, s0
	s_cmp_gt_i32 s3, -1
	s_cbranch_scc0 .LBB0_2207
	s_lshl_b32 s4, s3, 5
	s_cbranch_execz .LBB0_2208
	s_branch .LBB0_2209

.LBB0_2228:
	v_readlane_b32 s6, v253, 23
	v_readlane_b32 s7, v253, 24
	s_mov_b32 s88, s98
	s_cmp_lt_u32 s7, 39
	s_cbranch_scc1 .LBB0_2278
	v_readlane_b32 s0, v253, 20
	s_waitcnt vmcnt(0)
	s_lshl_b32 s0, s0, 6
	s_sub_i32 s0, 0, s0
	s_barrier
	v_mbcnt_lo_u32_b32 v0, -1, 0
	v_mbcnt_hi_u32_b32 v0, -1, v0
	s_nop 0
	v_cmp_eq_u32_e32 vcc, s0, v0
	s_and_saveexec_b64 s[0:1], vcc
	s_cbranch_execz .LBB0_2277
	s_add_i32 s2, 0, 0x20160
	v_mov_b32_e32 v0, s2
	s_waitcnt vmcnt(0) expcnt(0) lgkmcnt(0)
	ds_read_b32 v2, v0
	s_add_i32 s2, 0, 0x20164
	v_mov_b32_e32 v0, s2
	ds_read_b32 v0, v0
	s_waitcnt lgkmcnt(1)
	v_cmp_ne_u32_e32 vcc, 0, v2
	s_cbranch_vccnz .LBB0_2245
	v_readlane_b32 s2, v253, 0
	v_readlane_b32 s3, v253, 1
	s_load_dwordx2 s[6:7], s[2:3], 0x4
	s_add_u32 s2, s94, 0x4200
	s_addc_u32 s3, s95, 0
	s_add_u32 s4, s94, 0x4400
	s_addc_u32 s5, s95, 0
	s_waitcnt lgkmcnt(0)
	s_mul_i32 s33, s6, s90
	s_add_u32 s6, s94, 0x4500
	s_mul_i32 s33, s33, s7
	s_addc_u32 s7, s95, 0
	s_add_u32 s8, s94, 0x4600
	s_addc_u32 s9, s95, 0
	s_add_u32 s10, s94, 0x4700
	s_addc_u32 s11, s95, 0
	s_add_u32 s12, s94, 0x4800
	s_addc_u32 s13, s95, 0
	s_add_u32 s14, s94, 0x4900
	s_addc_u32 s15, s95, 0
	s_add_u32 s16, s94, 0x4a00
	s_addc_u32 s17, s95, 0
	s_add_u32 s18, s94, 0x4b00
	s_addc_u32 s19, s95, 0
	s_add_u32 s20, s94, 0x4c00
	s_addc_u32 s21, s95, 0
	s_add_u32 s22, s94, 0x4d00
	s_addc_u32 s23, s95, 0
	s_add_u32 s24, s94, 0x4e00
	s_addc_u32 s25, s95, 0
	s_add_u32 s26, s94, 0x4f00
	s_addc_u32 s27, s95, 0
	s_add_u32 s28, s94, 0x5000
	s_addc_u32 s29, s95, 0
	s_add_u32 s30, s94, 0x5100
	s_addc_u32 s31, s95, 0
	s_add_u32 s34, s94, 0x5200
	s_addc_u32 s35, s95, 0
	s_add_u32 s36, s94, 0x5300
	s_addc_u32 s37, s95, 0
	s_mov_b32 s44, 1
	v_mov_b32_e32 v16, 0
	s_branch .LBB0_2233

.LBB0_2278:
	s_cmp_gt_i32 s6, 38
	s_cselect_b64 s[0:1], -1, 0
	s_cmp_lt_i32 s7, 39
	s_cselect_b64 s[2:3], -1, 0
	s_or_b64 s[0:1], s[0:1], s[2:3]
	s_and_b64 vcc, exec, s[0:1]
	s_cbranch_vccnz .LBB0_2353
	s_mov_b32 s98, s88
	s_and_b32 s99, s88, 31
	s_lshl_b32 s99, s99, 3
	s_lshr_b32 s88, s88, 5
	s_or_b32 s88, s88, s99
	s_cmpk_gt_i32 s88, 0xff
	s_waitcnt vmcnt(0)
	v_mbcnt_lo_u32_b32 v0, -1, 0
	v_mbcnt_hi_u32_b32 v0, -1, v0
	v_mbcnt_lo_u32_b32 v8, -1, 0
	v_mbcnt_hi_u32_b32 v8, -1, v8
	s_cbranch_scc1 .LBB0_2303
	s_ashr_i32 s28, s88, 31
	s_lshr_b32 s0, s28, 29
	s_add_i32 s3, s88, s0
	s_and_b32 s0, s3, -8
	s_sub_i32 s4, s88, s0
	s_cmp_gt_i32 s4, -1
	s_cbranch_scc0 .LBB0_2282
	s_lshl_b32 s2, s4, 5
	s_cbranch_execz .LBB0_2283
	s_branch .LBB0_2284

.LBB0_2303:
	v_readlane_b32 s6, v253, 23
	v_readlane_b32 s7, v253, 24
	s_mov_b32 s88, s98
	s_cmp_lt_u32 s7, 40
	s_cbranch_scc1 .LBB0_2353
	v_readlane_b32 s0, v253, 20
	s_waitcnt vmcnt(0)
	s_lshl_b32 s0, s0, 6
	s_sub_i32 s0, 0, s0
	s_waitcnt vmcnt(0)
	s_barrier
	v_mbcnt_lo_u32_b32 v0, -1, 0
	v_mbcnt_hi_u32_b32 v0, -1, v0
	s_nop 0
	v_cmp_eq_u32_e32 vcc, s0, v0
	s_and_saveexec_b64 s[0:1], vcc
	s_cbranch_execz .LBB0_2352
	s_add_i32 s2, 0, 0x20160
	v_mov_b32_e32 v0, s2
	s_waitcnt vmcnt(0) expcnt(0) lgkmcnt(0)
	ds_read_b32 v2, v0
	s_add_i32 s2, 0, 0x20164
	v_mov_b32_e32 v0, s2
	ds_read_b32 v0, v0
	s_waitcnt lgkmcnt(1)
	v_cmp_ne_u32_e32 vcc, 0, v2
	s_cbranch_vccnz .LBB0_2320
	v_readlane_b32 s2, v253, 0
	v_readlane_b32 s3, v253, 1
	s_load_dwordx2 s[6:7], s[2:3], 0x4
	s_add_u32 s2, s94, 0x4200
	s_addc_u32 s3, s95, 0
	s_add_u32 s4, s94, 0x4400
	s_addc_u32 s5, s95, 0
	s_waitcnt lgkmcnt(0)
	s_mul_i32 s33, s6, s90
	s_add_u32 s6, s94, 0x4500
	s_mul_i32 s33, s33, s7
	s_addc_u32 s7, s95, 0
	s_add_u32 s8, s94, 0x4600
	s_addc_u32 s9, s95, 0
	s_add_u32 s10, s94, 0x4700
	s_addc_u32 s11, s95, 0
	s_add_u32 s12, s94, 0x4800
	s_addc_u32 s13, s95, 0
	s_add_u32 s14, s94, 0x4900
	s_addc_u32 s15, s95, 0
	s_add_u32 s16, s94, 0x4a00
	s_addc_u32 s17, s95, 0
	s_add_u32 s18, s94, 0x4b00
	s_addc_u32 s19, s95, 0
	s_add_u32 s20, s94, 0x4c00
	s_addc_u32 s21, s95, 0
	s_add_u32 s22, s94, 0x4d00
	s_addc_u32 s23, s95, 0
	s_add_u32 s24, s94, 0x4e00
	s_addc_u32 s25, s95, 0
	s_add_u32 s26, s94, 0x4f00
	s_addc_u32 s27, s95, 0
	s_add_u32 s28, s94, 0x5000
	s_addc_u32 s29, s95, 0
	s_add_u32 s30, s94, 0x5100
	s_addc_u32 s31, s95, 0
	s_add_u32 s34, s94, 0x5200
	s_addc_u32 s35, s95, 0
	s_add_u32 s36, s94, 0x5300
	s_addc_u32 s37, s95, 0
	s_mov_b32 s44, 1
	v_mov_b32_e32 v16, 0
	s_branch .LBB0_2308

.LBB0_2635:
	s_cmp_gt_i32 s6, 41
	s_cselect_b64 s[0:1], -1, 0
	s_cmp_lt_i32 s7, 42
	s_cselect_b64 s[2:3], -1, 0
	s_or_b64 s[0:1], s[0:1], s[2:3]
	s_and_b64 vcc, exec, s[0:1]
	s_cbranch_vccnz .LBB0_2769
	s_mov_b32 s98, s88
	s_and_b32 s99, s88, 31
	s_lshl_b32 s99, s99, 3
	s_lshr_b32 s88, s88, 5
	s_or_b32 s88, s88, s99
	s_waitcnt vmcnt(0)
	v_mov_b32_e32 v1, 0x420000
	v_mbcnt_lo_u32_b32 v0, -1, 0
	v_mbcnt_hi_u32_b32 v0, -1, v0
	global_load_dword v1, v1, s[94:95]
	s_and_b32 s0, s89, 0xffffffc0
	s_movk_i32 s1, 0x140
	v_add_u32_e32 v0, s0, v0
	s_add_u32 s2, s94, 0x420000
	s_addc_u32 s3, s95, 0
	v_cmp_gt_i32_e32 vcc, s1, v0
	s_waitcnt vmcnt(0)
	v_readfirstlane_b32 s41, v1
	s_and_saveexec_b64 s[0:1], vcc
	s_cbranch_execz .LBB0_2638
	v_ashrrev_i32_e32 v1, 31, v0
	v_lshl_add_u64 v[2:3], v[0:1], 2, s[2:3]
	global_load_dword v1, v[2:3], off offset:4
	v_lshl_add_u32 v2, v0, 2, 0
	v_add_u32_e32 v2, 0x22400, v2
	s_waitcnt vmcnt(0)
	ds_write_b32 v2, v1

.LBB0_2719:
	v_readlane_b32 s6, v253, 23
	v_readlane_b32 s7, v253, 24
	s_mov_b32 s88, s98
	s_cmp_lt_u32 s7, 43
	s_waitcnt vmcnt(0)
	s_barrier
	s_cbranch_scc1 .LBB0_2769
	v_readlane_b32 s0, v253, 20
	s_waitcnt vmcnt(0)
	s_lshl_b32 s0, s0, 6
	s_sub_i32 s0, 0, s0
	s_barrier
	v_mbcnt_lo_u32_b32 v0, -1, 0
	v_mbcnt_hi_u32_b32 v0, -1, v0
	s_nop 0
	v_cmp_eq_u32_e32 vcc, s0, v0
	s_and_saveexec_b64 s[0:1], vcc
	s_cbranch_execz .LBB0_2768
	s_add_i32 s2, 0, 0x20160
	v_mov_b32_e32 v0, s2
	s_waitcnt vmcnt(0) expcnt(0) lgkmcnt(0)
	ds_read_b32 v2, v0
	s_add_i32 s2, 0, 0x20164
	v_mov_b32_e32 v0, s2
	ds_read_b32 v0, v0
	s_waitcnt lgkmcnt(1)
	v_cmp_ne_u32_e32 vcc, 0, v2
	s_cbranch_vccnz .LBB0_2736
	v_readlane_b32 s2, v253, 0
	v_readlane_b32 s3, v253, 1
	s_load_dwordx2 s[6:7], s[2:3], 0x4
	s_add_u32 s2, s94, 0x4200
	s_addc_u32 s3, s95, 0
	s_add_u32 s4, s94, 0x4400
	s_addc_u32 s5, s95, 0
	s_waitcnt lgkmcnt(0)
	s_mul_i32 s33, s6, s90
	s_add_u32 s6, s94, 0x4500
	s_mul_i32 s33, s33, s7
	s_addc_u32 s7, s95, 0
	s_add_u32 s8, s94, 0x4600
	s_addc_u32 s9, s95, 0
	s_add_u32 s10, s94, 0x4700
	s_addc_u32 s11, s95, 0
	s_add_u32 s12, s94, 0x4800
	s_addc_u32 s13, s95, 0
	s_add_u32 s14, s94, 0x4900
	s_addc_u32 s15, s95, 0
	s_add_u32 s16, s94, 0x4a00
	s_addc_u32 s17, s95, 0
	s_add_u32 s18, s94, 0x4b00
	s_addc_u32 s19, s95, 0
	s_add_u32 s20, s94, 0x4c00
	s_addc_u32 s21, s95, 0
	s_add_u32 s22, s94, 0x4d00
	s_addc_u32 s23, s95, 0
	s_add_u32 s24, s94, 0x4e00
	s_addc_u32 s25, s95, 0
	s_add_u32 s26, s94, 0x4f00
	s_addc_u32 s27, s95, 0
	s_add_u32 s28, s94, 0x5000
	s_addc_u32 s29, s95, 0
	s_add_u32 s30, s94, 0x5100
	s_addc_u32 s31, s95, 0
	s_add_u32 s34, s94, 0x5200
	s_addc_u32 s35, s95, 0
	s_add_u32 s36, s94, 0x5300
	s_addc_u32 s37, s95, 0
	s_mov_b32 s44, 1
	v_mov_b32_e32 v16, 0
	s_branch .LBB0_2724

.LBB0_2769:
	s_cmp_gt_i32 s6, 42
	s_cselect_b64 s[0:1], -1, 0
	s_cmp_lt_i32 s7, 43
	s_cselect_b64 s[2:3], -1, 0
	s_or_b64 s[0:1], s[0:1], s[2:3]
	s_and_b64 vcc, exec, s[0:1]
	s_cbranch_vccnz .LBB0_2867
	s_mov_b32 s98, s88
	s_and_b32 s99, s88, 31
	s_lshl_b32 s99, s99, 3
	s_lshr_b32 s88, s88, 5
	s_or_b32 s88, s88, s99
	s_waitcnt vmcnt(0)
	v_mov_b32_e32 v1, 0x420000
	v_mbcnt_lo_u32_b32 v0, -1, 0
	v_mbcnt_hi_u32_b32 v0, -1, v0
	global_load_dword v1, v1, s[94:95]
	s_and_b32 s0, s89, 0xffffffc0
	s_movk_i32 s1, 0x140
	v_add_u32_e32 v0, s0, v0
	s_add_u32 s2, s94, 0x420000
	s_addc_u32 s3, s95, 0
	v_cmp_gt_i32_e32 vcc, s1, v0
	s_waitcnt vmcnt(0)
	v_readfirstlane_b32 s44, v1
	s_and_saveexec_b64 s[0:1], vcc
	s_cbranch_execz .LBB0_2772
	v_ashrrev_i32_e32 v1, 31, v0
	v_lshl_add_u64 v[2:3], v[0:1], 2, s[2:3]
	global_load_dword v1, v[2:3], off offset:4
	v_lshl_add_u32 v0, v0, 2, 0
	v_add_u32_e32 v0, 0x22400, v0
	s_waitcnt vmcnt(0)
	ds_write_b32 v0, v1

.LBB0_2817:
	v_readlane_b32 s6, v253, 23
	v_readlane_b32 s7, v253, 24
	s_mov_b32 s88, s98
	s_cmp_lt_u32 s7, 44
	s_waitcnt vmcnt(0)
	s_barrier
	s_cbranch_scc1 .LBB0_2867
	v_readlane_b32 s0, v253, 20
	s_waitcnt vmcnt(0)
	s_lshl_b32 s0, s0, 6
	s_sub_i32 s0, 0, s0
	s_barrier
	v_mbcnt_lo_u32_b32 v0, -1, 0
	v_mbcnt_hi_u32_b32 v0, -1, v0
	s_nop 0
	v_cmp_eq_u32_e32 vcc, s0, v0
	s_and_saveexec_b64 s[0:1], vcc
	s_cbranch_execz .LBB0_2866
	s_add_i32 s2, 0, 0x20160
	v_mov_b32_e32 v0, s2
	s_waitcnt vmcnt(0) expcnt(0) lgkmcnt(0)
	ds_read_b32 v2, v0
	s_add_i32 s2, 0, 0x20164
	v_mov_b32_e32 v0, s2
	ds_read_b32 v0, v0
	s_waitcnt lgkmcnt(1)
	v_cmp_ne_u32_e32 vcc, 0, v2
	s_cbranch_vccnz .LBB0_2834
	v_readlane_b32 s2, v253, 0
	v_readlane_b32 s3, v253, 1
	s_load_dwordx2 s[6:7], s[2:3], 0x4
	s_add_u32 s2, s94, 0x4200
	s_addc_u32 s3, s95, 0
	s_add_u32 s4, s94, 0x4400
	s_addc_u32 s5, s95, 0
	s_waitcnt lgkmcnt(0)
	s_mul_i32 s33, s6, s90
	s_add_u32 s6, s94, 0x4500
	s_mul_i32 s33, s33, s7
	s_addc_u32 s7, s95, 0
	s_add_u32 s8, s94, 0x4600
	s_addc_u32 s9, s95, 0
	s_add_u32 s10, s94, 0x4700
	s_addc_u32 s11, s95, 0
	s_add_u32 s12, s94, 0x4800
	s_addc_u32 s13, s95, 0
	s_add_u32 s14, s94, 0x4900
	s_addc_u32 s15, s95, 0
	s_add_u32 s16, s94, 0x4a00
	s_addc_u32 s17, s95, 0
	s_add_u32 s18, s94, 0x4b00
	s_addc_u32 s19, s95, 0
	s_add_u32 s20, s94, 0x4c00
	s_addc_u32 s21, s95, 0
	s_add_u32 s22, s94, 0x4d00
	s_addc_u32 s23, s95, 0
	s_add_u32 s24, s94, 0x4e00
	s_addc_u32 s25, s95, 0
	s_add_u32 s26, s94, 0x4f00
	s_addc_u32 s27, s95, 0
	s_add_u32 s28, s94, 0x5000
	s_addc_u32 s29, s95, 0
	s_add_u32 s30, s94, 0x5100
	s_addc_u32 s31, s95, 0
	s_add_u32 s34, s94, 0x5200
	s_addc_u32 s35, s95, 0
	s_add_u32 s36, s94, 0x5300
	s_addc_u32 s37, s95, 0
	s_mov_b32 s44, 1
	v_mov_b32_e32 v16, 0
	s_branch .LBB0_2822

.LBB0_2943:
	s_cmp_gt_i32 s6, 50
	s_cselect_b64 s[0:1], -1, 0
	s_cmp_lt_i32 s7, 51
	s_cselect_b64 s[2:3], -1, 0
	s_or_b64 s[0:1], s[0:1], s[2:3]
	s_and_b64 vcc, exec, s[0:1]
	s_cbranch_vccnz .LBB0_3010
	s_mov_b32 s98, s88
	s_and_b32 s99, s88, 31
	s_lshl_b32 s99, s99, 3
	s_lshr_b32 s88, s88, 5
	s_or_b32 s88, s88, s99
	s_cmpk_gt_i32 s88, 0x4ff
	s_waitcnt vmcnt(0)
	v_mbcnt_lo_u32_b32 v0, -1, 0
	v_mbcnt_hi_u32_b32 v0, -1, v0
	v_mbcnt_lo_u32_b32 v6, -1, 0
	v_mbcnt_hi_u32_b32 v6, -1, v6
	s_cbranch_scc1 .LBB0_2960
	s_add_u32 s11, s94, 0x37600000
	s_addc_u32 s30, s95, 0
	s_add_u32 s31, s94, 0x1200000
	v_readlane_b32 s0, v253, 20
	s_addc_u32 s34, s95, 0
	s_lshl_b32 s35, s0, 10
	v_lshl_add_u32 v0, v6, 4, s35
	v_add_u32_e32 v1, 0x2000, v0
	v_ashrrev_i32_e32 v2, 31, v1
	v_lshrrev_b32_e32 v2, 22, v2
	v_add_u32_e32 v2, v1, v2
	v_ashrrev_i32_e32 v4, 10, v2
	v_mul_i32_i24_e32 v2, 0x400, v4
	v_sub_u32_e32 v1, v1, v2
	v_lshrrev_b32_e32 v2, 4, v1
	v_bitop3_b32 v1, v2, v1, 32 bitop3:0x6c
	v_ashrrev_i32_e32 v2, 31, v1
	v_lshrrev_b32_e32 v2, 26, v2
	v_add_u32_e32 v2, v1, v2
	v_ashrrev_i32_e32 v5, 6, v2
	v_lshlrev_b32_e32 v3, 3, v4
	v_and_b32_e32 v2, 0xffc0, v2
	v_and_b32_e32 v3, -16, v3
	v_sub_u32_e32 v1, v1, v2
	v_add_u32_e32 v3, v5, v3
	v_lshrrev_b16_e32 v2, 7, v1
	v_and_b32_e32 v7, 3, v5
	s_mov_b32 s0, 0x1ffffe0
	v_lshrrev_b32_e32 v8, 2, v3
	v_lshlrev_b32_e32 v9, 1, v3
	v_and_b32_e32 v2, 1, v2
	v_and_or_b32 v7, v3, s0, v7
	v_and_b32_e32 v8, 4, v8
	v_and_b32_e32 v9, 24, v9
	v_add_u16_e32 v1, v1, v2
	v_mov_b32_e32 v2, 1
	v_or3_b32 v8, v7, v8, v9
	v_lshlrev_b32_e32 v7, 5, v4
	v_ashrrev_i16_sdwa v1, v2, sext(v1) dst_sel:DWORD dst_unused:UNUSED_PAD src0_sel:DWORD src1_sel:BYTE_0
	v_and_b32_e32 v9, 32, v7
	v_bfe_i32 v7, v1, 0, 16
	v_add_lshl_u32 v1, v9, v7, 1
	v_lshl_add_u32 v160, v8, 7, v1
	v_lshl_add_u32 v162, v3, 10, v1
	v_ashrrev_i32_e32 v1, 31, v0
	v_lshrrev_b32_e32 v1, 22, v1
	v_add_u32_e32 v1, v0, v1
	v_ashrrev_i32_e32 v8, 10, v1
	v_mul_i32_i24_e32 v1, 0x400, v8
	v_sub_u32_e32 v0, v0, v1
	v_lshrrev_b32_e32 v1, 4, v0
	v_bitop3_b32 v0, v1, v0, 32 bitop3:0x6c
	v_ashrrev_i32_e32 v1, 31, v0
	v_lshrrev_b32_e32 v1, 26, v1
	v_add_u32_e32 v1, v0, v1
	v_lshlrev_b32_e32 v3, 3, v8
	v_ashrrev_i32_e32 v9, 6, v1
	v_and_b32_e32 v3, -16, v3
	v_add_u32_e32 v3, v9, v3
	v_and_b32_e32 v10, 3, v9
	s_ashr_i32 s36, s88, 31
	v_and_or_b32 v10, v3, s0, v10
	s_lshr_b32 s0, s36, 29
	s_add_i32 s0, s88, s0
	s_ashr_i32 s2, s0, 3
	s_and_b32 s0, s0, -8
	s_lshr_b32 s1, s89, 8
	s_sub_i32 s0, s88, s0
	s_cmp_lt_i32 s0, 0
	s_movk_i32 s37, 0xa1
	s_cselect_b32 s3, s37, 0xa0
	s_mul_i32 s0, s3, s0
	s_add_i32 s0, s0, s2
	s_mul_hi_i32 s2, s0, 0x66666667
	s_lshr_b32 s3, s2, 31
	s_ashr_i32 s2, s2, 9
	s_add_i32 s2, s2, s3
	s_mulk_i32 s2, 0x500
	s_sub_i32 s0, s0, s2
	s_sext_i32_i16 s2, s0
	s_mulk_i32 s2, 0x6667
	s_lshr_b32 s3, s2, 31
	s_ashr_i32 s2, s2, 22
	s_add_i32 s2, s2, s3
	s_lshl_b32 s3, s2, 3
	s_mulk_i32 s2, 0xa0
	s_sub_i32 s2, s0, s2
	s_sext_i32_i16 s0, s2
	s_bfe_u32 s0, s0, 0x3001c
	s_add_i32 s4, s2, s0
	s_sext_i32_i16 s0, s4
	s_and_b32 s4, s4, 0xfff8
	s_sub_i32 s2, s2, s4
	s_sext_i32_i16 s2, s2
	v_lshrrev_b32_e32 v11, 2, v3
	v_lshlrev_b32_e32 v12, 1, v3
	v_and_b32_e32 v1, 0xc0, v1
	s_lshr_b32 s0, s0, 3
	s_add_i32 s2, s3, s2
	v_and_b32_e32 v11, 4, v11
	v_and_b32_e32 v12, 24, v12
	v_sub_u32_e32 v0, v0, v1
	s_ashr_i32 s3, s2, 31
	s_bfe_i64 s[4:5], s[0:1], 0x100000
	v_or3_b32 v11, v10, v11, v12
	v_lshlrev_b32_e32 v10, 5, v8
	v_ashrrev_i16_sdwa v0, v2, sext(v0) dst_sel:DWORD dst_unused:UNUSED_PAD src0_sel:DWORD src1_sel:BYTE_0
	s_lshl_b64 s[4:5], s[4:5], 18
	s_lshl_b64 s[6:7], s[2:3], 18
	v_and_b32_e32 v12, 32, v10
	v_bfe_i32 v10, v0, 0, 16
	s_add_u32 s24, s31, s4
	v_add_lshl_u32 v0, v12, v10, 1
	s_addc_u32 s25, s34, s5
	s_add_i32 s38, s35, 0
	v_lshl_add_u32 v164, v11, 7, v0
	s_add_i32 m0, s38, 0x10000
	v_lshl_add_u32 v166, v3, 10, v0
	global_load_lds_dwordx4 v164, s[24:25]
	s_add_i32 m0, s38, 0x12000
	s_add_u32 s4, s24, 0x4000
	global_load_lds_dwordx4 v160, s[24:25]
	s_addc_u32 s5, s25, 0
	s_add_i32 m0, s38, 0x14000
	v_mov_b32_e32 v169, 0
	global_load_lds_dwordx4 v164, s[4:5]
	s_add_i32 m0, s38, 0x16000
	s_add_u32 s26, s11, s6
	s_addc_u32 s27, s30, s7
	s_add_i32 s39, s38, 0x2000
	global_load_lds_dwordx4 v160, s[4:5]
	s_mov_b32 m0, s38
	s_add_u32 s4, s26, 0x20000
	global_load_lds_dwordx4 v166, s[26:27]
	s_mov_b32 m0, s39
	s_addc_u32 s5, s27, 0
	s_add_i32 s40, s38, 0x4000
	global_load_lds_dwordx4 v162, s[26:27]
	s_mov_b32 m0, s40
	s_add_i32 s41, s38, 0x6000
	global_load_lds_dwordx4 v166, s[4:5]
	s_mov_b32 m0, s41
	v_mov_b32_e32 v167, v169
	global_load_lds_dwordx4 v162, s[4:5]
	v_mov_b32_e32 v163, v169
	s_cmp_eq_u32 s1, 1
	s_mov_b32 s3, 0
	v_mov_b32_e32 v165, v169
	v_mov_b32_e32 v161, v169
	v_lshl_add_u64 v[0:1], s[26:27], 0, v[166:167]
	s_cselect_b64 s[4:5], -1, 0
	s_cmp_lg_u32 s1, 1
	v_lshl_add_u64 v[2:3], s[26:27], 0, v[162:163]
	s_cbranch_scc1 .LBB0_2947
	s_barrier

.LBB0_2960:
	v_readlane_b32 s6, v253, 23
	v_readlane_b32 s7, v253, 24
	s_mov_b32 s88, s98
	s_cmp_lt_u32 s7, 52
	s_cbranch_scc1 .LBB0_3010
	v_readlane_b32 s0, v253, 20
	s_waitcnt vmcnt(0)
	s_lshl_b32 s0, s0, 6
	s_sub_i32 s0, 0, s0
	s_waitcnt vmcnt(0)
	s_barrier
	v_mbcnt_lo_u32_b32 v0, -1, 0
	v_mbcnt_hi_u32_b32 v0, -1, v0
	s_nop 0
	v_cmp_eq_u32_e32 vcc, s0, v0
	s_and_saveexec_b64 s[0:1], vcc
	s_cbranch_execz .LBB0_3009
	s_add_i32 s2, 0, 0x20160
	v_mov_b32_e32 v0, s2
	s_waitcnt vmcnt(0) expcnt(0) lgkmcnt(0)
	ds_read_b32 v2, v0
	s_add_i32 s2, 0, 0x20164
	v_mov_b32_e32 v0, s2
	ds_read_b32 v0, v0
	s_waitcnt lgkmcnt(1)
	v_cmp_ne_u32_e32 vcc, 0, v2
	s_cbranch_vccnz .LBB0_2977
	v_readlane_b32 s2, v253, 0
	v_readlane_b32 s3, v253, 1
	s_load_dwordx2 s[6:7], s[2:3], 0x4
	s_add_u32 s2, s94, 0x4200
	s_addc_u32 s3, s95, 0
	s_add_u32 s4, s94, 0x4400
	s_addc_u32 s5, s95, 0
	s_waitcnt lgkmcnt(0)
	s_mul_i32 s33, s6, s90
	s_add_u32 s6, s94, 0x4500
	s_mul_i32 s33, s33, s7
	s_addc_u32 s7, s95, 0
	s_add_u32 s8, s94, 0x4600
	s_addc_u32 s9, s95, 0
	s_add_u32 s10, s94, 0x4700
	s_addc_u32 s11, s95, 0
	s_add_u32 s12, s94, 0x4800
	s_addc_u32 s13, s95, 0
	s_add_u32 s14, s94, 0x4900
	s_addc_u32 s15, s95, 0
	s_add_u32 s16, s94, 0x4a00
	s_addc_u32 s17, s95, 0
	s_add_u32 s18, s94, 0x4b00
	s_addc_u32 s19, s95, 0
	s_add_u32 s20, s94, 0x4c00
	s_addc_u32 s21, s95, 0
	s_add_u32 s22, s94, 0x4d00
	s_addc_u32 s23, s95, 0
	s_add_u32 s24, s94, 0x4e00
	s_addc_u32 s25, s95, 0
	s_add_u32 s26, s94, 0x4f00
	s_addc_u32 s27, s95, 0
	s_add_u32 s28, s94, 0x5000
	s_addc_u32 s29, s95, 0
	s_add_u32 s30, s94, 0x5100
	s_addc_u32 s31, s95, 0
	s_add_u32 s34, s94, 0x5200
	s_addc_u32 s35, s95, 0
	s_add_u32 s36, s94, 0x5300
	s_addc_u32 s37, s95, 0
	s_mov_b32 s44, 1
	v_mov_b32_e32 v16, 0
	s_branch .LBB0_2965

.LBB0_3225:
	s_cmp_gt_i32 s6, 54
	s_cselect_b64 s[0:1], -1, 0
	s_cmp_lt_i32 s7, 55
	s_cselect_b64 s[2:3], -1, 0
	s_or_b64 s[0:1], s[0:1], s[2:3]
	s_and_b64 vcc, exec, s[0:1]
	s_cbranch_vccnz .LBB0_3300
	s_mov_b32 s98, s88
	s_and_b32 s99, s88, 31
	s_lshl_b32 s99, s99, 3
	s_lshr_b32 s88, s88, 5
	s_or_b32 s88, s88, s99
	s_cmpk_gt_i32 s88, 0xff
	s_waitcnt vmcnt(0)
	v_mbcnt_lo_u32_b32 v0, -1, 0
	v_mbcnt_hi_u32_b32 v0, -1, v0
	v_mbcnt_lo_u32_b32 v8, -1, 0
	v_mbcnt_hi_u32_b32 v8, -1, v8
	s_cbranch_scc1 .LBB0_3250
	s_ashr_i32 s28, s88, 31
	s_lshr_b32 s0, s28, 29
	s_add_i32 s3, s88, s0
	s_and_b32 s0, s3, -8
	s_sub_i32 s4, s88, s0
	s_cmp_gt_i32 s4, -1
	s_cbranch_scc0 .LBB0_3229
	s_lshl_b32 s2, s4, 5
	s_cbranch_execz .LBB0_3230
	s_branch .LBB0_3231

.LBB0_3250:
	v_readlane_b32 s6, v253, 23
	v_readlane_b32 s7, v253, 24
	s_mov_b32 s88, s98
	s_cmp_lt_u32 s7, 56
	s_cbranch_scc1 .LBB0_3300
	v_readlane_b32 s0, v253, 20
	s_waitcnt vmcnt(0)
	s_lshl_b32 s0, s0, 6
	s_sub_i32 s0, 0, s0
	s_waitcnt vmcnt(0)
	s_barrier
	v_mbcnt_lo_u32_b32 v0, -1, 0
	v_mbcnt_hi_u32_b32 v0, -1, v0
	s_nop 0
	v_cmp_eq_u32_e32 vcc, s0, v0
	s_and_saveexec_b64 s[0:1], vcc
	s_cbranch_execz .LBB0_3299
	s_add_i32 s2, 0, 0x20160
	v_mov_b32_e32 v0, s2
	s_waitcnt vmcnt(0) expcnt(0) lgkmcnt(0)
	ds_read_b32 v2, v0
	s_add_i32 s2, 0, 0x20164
	v_mov_b32_e32 v0, s2
	ds_read_b32 v0, v0
	s_waitcnt lgkmcnt(1)
	v_cmp_ne_u32_e32 vcc, 0, v2
	s_cbranch_vccnz .LBB0_3267
	v_readlane_b32 s2, v253, 0
	v_readlane_b32 s3, v253, 1
	s_load_dwordx2 s[6:7], s[2:3], 0x4
	s_add_u32 s2, s94, 0x4200
	s_addc_u32 s3, s95, 0
	s_add_u32 s4, s94, 0x4400
	s_addc_u32 s5, s95, 0
	s_waitcnt lgkmcnt(0)
	s_mul_i32 s33, s6, s90
	s_add_u32 s6, s94, 0x4500
	s_mul_i32 s33, s33, s7
	s_addc_u32 s7, s95, 0
	s_add_u32 s8, s94, 0x4600
	s_addc_u32 s9, s95, 0
	s_add_u32 s10, s94, 0x4700
	s_addc_u32 s11, s95, 0
	s_add_u32 s12, s94, 0x4800
	s_addc_u32 s13, s95, 0
	s_add_u32 s14, s94, 0x4900
	s_addc_u32 s15, s95, 0
	s_add_u32 s16, s94, 0x4a00
	s_addc_u32 s17, s95, 0
	s_add_u32 s18, s94, 0x4b00
	s_addc_u32 s19, s95, 0
	s_add_u32 s20, s94, 0x4c00
	s_addc_u32 s21, s95, 0
	s_add_u32 s22, s94, 0x4d00
	s_addc_u32 s23, s95, 0
	s_add_u32 s24, s94, 0x4e00
	s_addc_u32 s25, s95, 0
	s_add_u32 s26, s94, 0x4f00
	s_addc_u32 s27, s95, 0
	s_add_u32 s28, s94, 0x5000
	s_addc_u32 s29, s95, 0
	s_add_u32 s30, s94, 0x5100
	s_addc_u32 s31, s95, 0
	s_add_u32 s34, s94, 0x5200
	s_addc_u32 s35, s95, 0
	s_add_u32 s36, s94, 0x5300
	s_addc_u32 s37, s95, 0
	s_mov_b32 s44, 1
	v_mov_b32_e32 v16, 0
	s_branch .LBB0_3255

.LBB0_3598:
	s_cmp_gt_i32 s6, 57
	s_cselect_b64 s[0:1], -1, 0
	s_cmp_lt_i32 s7, 58
	s_cselect_b64 s[2:3], -1, 0
	s_or_b64 s[0:1], s[0:1], s[2:3]
	s_and_b64 vcc, exec, s[0:1]
	s_cbranch_vccnz .LBB0_3713
	s_mov_b32 s98, s88
	s_and_b32 s99, s88, 31
	s_lshl_b32 s99, s99, 3
	s_lshr_b32 s88, s88, 5
	s_or_b32 s88, s88, s99
	s_waitcnt vmcnt(0)
	v_mov_b32_e32 v1, 0x420000
	v_mbcnt_lo_u32_b32 v0, -1, 0
	v_mbcnt_hi_u32_b32 v0, -1, v0
	global_load_dword v1, v1, s[94:95]
	s_and_b32 s0, s89, 0xffffffc0
	s_movk_i32 s1, 0x140
	v_add_u32_e32 v0, s0, v0
	s_add_u32 s2, s94, 0x420000
	s_addc_u32 s3, s95, 0
	v_cmp_gt_i32_e32 vcc, s1, v0
	s_waitcnt vmcnt(0)
	v_readfirstlane_b32 s17, v1
	s_and_saveexec_b64 s[0:1], vcc
	s_cbranch_execz .LBB0_3601
	v_ashrrev_i32_e32 v1, 31, v0
	v_lshl_add_u64 v[2:3], v[0:1], 2, s[2:3]
	global_load_dword v1, v[2:3], off offset:4
	v_lshl_add_u32 v2, v0, 2, 0
	v_add_u32_e32 v2, 0x22400, v2
	s_waitcnt vmcnt(0)
	ds_write_b32 v2, v1

.LBB0_3663:
	v_readlane_b32 s6, v253, 23
	v_readlane_b32 s7, v253, 24
	s_mov_b32 s88, s98
	s_cmp_lt_u32 s7, 59
	s_cbranch_scc1 .LBB0_3713
	v_readlane_b32 s0, v253, 20
	s_waitcnt vmcnt(0)
	s_lshl_b32 s0, s0, 6
	s_sub_i32 s0, 0, s0
	s_waitcnt vmcnt(0)
	s_barrier
	v_mbcnt_lo_u32_b32 v0, -1, 0
	v_mbcnt_hi_u32_b32 v0, -1, v0
	s_nop 0
	v_cmp_eq_u32_e32 vcc, s0, v0
	s_and_saveexec_b64 s[0:1], vcc
	s_cbranch_execz .LBB0_3712
	s_add_i32 s2, 0, 0x20160
	v_mov_b32_e32 v0, s2
	s_waitcnt vmcnt(0) expcnt(0) lgkmcnt(0)
	ds_read_b32 v2, v0
	s_add_i32 s2, 0, 0x20164
	v_mov_b32_e32 v0, s2
	ds_read_b32 v0, v0
	s_waitcnt lgkmcnt(1)
	v_cmp_ne_u32_e32 vcc, 0, v2
	s_cbranch_vccnz .LBB0_3680
	v_readlane_b32 s2, v253, 0
	v_readlane_b32 s3, v253, 1
	s_load_dwordx2 s[6:7], s[2:3], 0x4
	s_add_u32 s2, s94, 0x4200
	s_addc_u32 s3, s95, 0
	s_add_u32 s4, s94, 0x4400
	s_addc_u32 s5, s95, 0
	s_waitcnt lgkmcnt(0)
	s_mul_i32 s33, s6, s90
	s_add_u32 s6, s94, 0x4500
	s_mul_i32 s33, s33, s7
	s_addc_u32 s7, s95, 0
	s_add_u32 s8, s94, 0x4600
	s_addc_u32 s9, s95, 0
	s_add_u32 s10, s94, 0x4700
	s_addc_u32 s11, s95, 0
	s_add_u32 s12, s94, 0x4800
	s_addc_u32 s13, s95, 0
	s_add_u32 s14, s94, 0x4900
	s_addc_u32 s15, s95, 0
	s_add_u32 s16, s94, 0x4a00
	s_addc_u32 s17, s95, 0
	s_add_u32 s18, s94, 0x4b00
	s_addc_u32 s19, s95, 0
	s_add_u32 s20, s94, 0x4c00
	s_addc_u32 s21, s95, 0
	s_add_u32 s22, s94, 0x4d00
	s_addc_u32 s23, s95, 0
	s_add_u32 s24, s94, 0x4e00
	s_addc_u32 s25, s95, 0
	s_add_u32 s26, s94, 0x4f00
	s_addc_u32 s27, s95, 0
	s_add_u32 s28, s94, 0x5000
	s_addc_u32 s29, s95, 0
	s_add_u32 s30, s94, 0x5100
	s_addc_u32 s31, s95, 0
	s_add_u32 s34, s94, 0x5200
	s_addc_u32 s35, s95, 0
	s_add_u32 s36, s94, 0x5300
	s_addc_u32 s37, s95, 0
	s_mov_b32 s44, 1
	v_mov_b32_e32 v16, 0
	s_branch .LBB0_3668

.LBB0_3713:
	s_cmp_gt_i32 s6, 58
	s_cselect_b64 s[0:1], -1, 0
	s_cmp_lt_i32 s7, 59
	s_cselect_b64 s[2:3], -1, 0
	s_or_b64 s[0:1], s[0:1], s[2:3]
	s_and_b64 vcc, exec, s[0:1]
	s_cbranch_vccnz .LBB0_3792
	s_mov_b32 s98, s88
	s_and_b32 s99, s88, 31
	s_lshl_b32 s99, s99, 3
	s_lshr_b32 s88, s88, 5
	s_or_b32 s88, s88, s99
	s_waitcnt vmcnt(0)
	v_mov_b32_e32 v1, 0x420000
	v_mbcnt_lo_u32_b32 v0, -1, 0
	v_mbcnt_hi_u32_b32 v0, -1, v0
	global_load_dword v1, v1, s[94:95]
	s_and_b32 s0, s89, 0xffffffc0
	s_movk_i32 s1, 0x140
	v_add_u32_e32 v0, s0, v0
	s_add_u32 s2, s94, 0x420000
	s_addc_u32 s3, s95, 0
	v_cmp_gt_i32_e32 vcc, s1, v0
	s_waitcnt vmcnt(0)
	v_readfirstlane_b32 s9, v1
	s_and_saveexec_b64 s[0:1], vcc
	s_cbranch_execz .LBB0_3716
	v_ashrrev_i32_e32 v1, 31, v0
	v_lshl_add_u64 v[2:3], v[0:1], 2, s[2:3]
	global_load_dword v1, v[2:3], off offset:4
	v_lshl_add_u32 v0, v0, 2, 0
	v_add_u32_e32 v0, 0x22400, v0
	s_waitcnt vmcnt(0)
	ds_write_b32 v0, v1

.LBB0_3742:
	v_readlane_b32 s6, v253, 23
	v_readlane_b32 s7, v253, 24
	s_mov_b32 s88, s98
	s_cmp_lt_u32 s7, 60
	s_cbranch_scc1 .LBB0_3792
	v_readlane_b32 s0, v253, 20
	s_waitcnt vmcnt(0)
	s_lshl_b32 s0, s0, 6
	s_sub_i32 s0, 0, s0
	s_waitcnt vmcnt(0)
	s_barrier
	v_mbcnt_lo_u32_b32 v0, -1, 0
	v_mbcnt_hi_u32_b32 v0, -1, v0
	s_nop 0
	v_cmp_eq_u32_e32 vcc, s0, v0
	s_and_saveexec_b64 s[0:1], vcc
	s_cbranch_execz .LBB0_3791
	s_add_i32 s2, 0, 0x20160
	v_mov_b32_e32 v0, s2
	s_waitcnt vmcnt(0) expcnt(0) lgkmcnt(0)
	ds_read_b32 v2, v0
	s_add_i32 s2, 0, 0x20164
	v_mov_b32_e32 v0, s2
	ds_read_b32 v0, v0
	s_waitcnt lgkmcnt(1)
	v_cmp_ne_u32_e32 vcc, 0, v2
	s_cbranch_vccnz .LBB0_3759
	v_readlane_b32 s2, v253, 0
	v_readlane_b32 s3, v253, 1
	s_load_dwordx2 s[6:7], s[2:3], 0x4
	s_add_u32 s2, s94, 0x4200
	s_addc_u32 s3, s95, 0
	s_add_u32 s4, s94, 0x4400
	s_addc_u32 s5, s95, 0
	s_waitcnt lgkmcnt(0)
	s_mul_i32 s33, s6, s90
	s_add_u32 s6, s94, 0x4500
	s_mul_i32 s33, s33, s7
	s_addc_u32 s7, s95, 0
	s_add_u32 s8, s94, 0x4600
	s_addc_u32 s9, s95, 0
	s_add_u32 s10, s94, 0x4700
	s_addc_u32 s11, s95, 0
	s_add_u32 s12, s94, 0x4800
	s_addc_u32 s13, s95, 0
	s_add_u32 s14, s94, 0x4900
	s_addc_u32 s15, s95, 0
	s_add_u32 s16, s94, 0x4a00
	s_addc_u32 s17, s95, 0
	s_add_u32 s18, s94, 0x4b00
	s_addc_u32 s19, s95, 0
	s_add_u32 s20, s94, 0x4c00
	s_addc_u32 s21, s95, 0
	s_add_u32 s22, s94, 0x4d00
	s_addc_u32 s23, s95, 0
	s_add_u32 s24, s94, 0x4e00
	s_addc_u32 s25, s95, 0
	s_add_u32 s26, s94, 0x4f00
	s_addc_u32 s27, s95, 0
	s_add_u32 s28, s94, 0x5000
	s_addc_u32 s29, s95, 0
	s_add_u32 s30, s94, 0x5100
	s_addc_u32 s31, s95, 0
	s_add_u32 s34, s94, 0x5200
	s_addc_u32 s35, s95, 0
	s_add_u32 s36, s94, 0x5300
	s_addc_u32 s37, s95, 0
	s_mov_b32 s44, 1
	v_mov_b32_e32 v16, 0
	s_branch .LBB0_3747
